# P6b pass U: token x rows go through four register sets (no LDS ring), lane reduction through the LDS matrix, one compare per step for token switch and staging
# speedup vs baseline: 1.0321x; 1.0037x over previous
; #define LAS __attribute__((address_space(3)))
; __device__ __forceinline__ void phase_peer_bucket(const Params& P, unsigned char* ws, int l, LAS unsigned char* lds, int bid, int G, int lane, int wave) {
;     LAS int* red = (LAS int*)lds + wave * (64 * 68);
;     const int x = bid & 7, r = bid >> 3;
;     const int u = r * 8 + wave; const unsigned nbase = (unsigned)u * 32u;
;     ...
;             const unsigned char* X1Q = ws + WS_X1Q;
;             float xsc_v = 0.f; if (lane < 32) xsc_v = ((const float*)(ws + WS_XSC))[nbase + lane];
;             int tcur = peer3_next_nonempty(gstv, 0); int tnx = peer3_next_nonempty(gstv, tcur + 1); int tend = __builtin_amdgcn_readlane(gstv, tcur + 1);
;             u4 xq[2];
;             { const unsigned char* p = X1Q + (size_t)(nbase + tcur) * 2048u + (unsigned)lane * 16u; xq[0] = __builtin_nontemporal_load((const u4*)p); xq[1] = __builtin_nontemporal_load((const u4*)(p + 1024)); }
;             int lt = tnx, lts = (lt < 32) ? __builtin_amdgcn_readlane(gstv, lt) : 0x7fffffff;
;             float xs = __int_as_float(__builtin_amdgcn_readlane(__float_as_int(xsc_v), tcur));
;             int evn = 0; float wvn = 0.f;
;             if (lane < total) { evn = __builtin_nontemporal_load(FE + lane); wvn = __builtin_nontemporal_load(FW + lane); }
.Lq_entry:
	s_mul_i32 s100, s29, 0x4400
	s_mov_b32 s65, 0x1010101
	s_mov_b32 s22, 0xf
	s_mov_b32 s23, 0
	v_mov_b32_e32 v117, 0x110
	v_mad_u32_u24 v107, v208, v117, s100
	v_lshl_add_u32 v108, v208, 2, s100
	s_add_u32 s52, s12, s14
	s_addc_u32 s53, s13, s15
	s_add_u32 s52, s52, 0xa000000
	s_addc_u32 s53, s53, 0
	s_sub_u32 s58, s16, 0x8000000
	s_subb_u32 s59, s17, 0
	v_readlane_b32 s4, v254, 52
	s_lshl_b32 s4, s4, 16
	s_add_u32 s18, s12, 0x4e000000
	s_addc_u32 s19, s13, 0
	s_add_u32 s18, s18, s4
	s_addc_u32 s19, s19, 0
	s_lshl_b32 s4, s8, 11
	s_add_u32 s26, s12, 0x6b000000
	s_addc_u32 s27, s13, 0
	s_add_u32 s26, s26, s4
	s_addc_u32 s27, s27, 0
	s_add_u32 s6, s12, 0x6c000000
	s_addc_u32 s7, s13, 0
	v_mov_b32_e32 v201, 0
	v_add_lshl_u32 v117, v208, s8, 2
	v_cmp_gt_u32_e32 vcc, 32, v208
	s_and_saveexec_b64 s[4:5], vcc
	global_load_dword v201, v117, s[6:7]
	s_or_b64 exec, exec, s[4:5]
	v_mov_b32_e32 v233, 0
	v_mov_b32_e32 v87, 0
	v_mov_b32_e32 v74, 0
	v_mov_b32_e32 v78, 0
	v_add_u32_e32 v118, 0x4000000, v212
	s_and_saveexec_b64 s[4:5], s[40:41]
	global_load_dword v74, v212, s[58:59] nt
	global_load_dword v78, v118, s[58:59] nt
	s_or_b64 exec, exec, s[4:5]
	s_mov_b32 s31, 0

; #define PU_SX() do { int a_ = 0, b_ = 0; _Pragma("unroll") for (int q_ = 0; q_ < 4; ++q_) { a_ = __builtin_amdgcn_sdot4((int)xq[0][q_], 0x01010101, a_, false); b_ = __builtin_amdgcn_sdot4((int)xq[1][q_], 0x01010101, b_, false); } sx15 = 240 * a_ - 16 * b_; } while (0)
; __device__ __forceinline__ void phase_peer_bucket(const Params& P, unsigned char* ws, int l, LAS unsigned char* lds, int bid, int G, int lane, int wave) {
;     ...
;             int tcur = peer3_next_nonempty(gstv, 0); int tnx = peer3_next_nonempty(gstv, tcur + 1); int tend = __builtin_amdgcn_readlane(gstv, tcur + 1);
;             u4 xq[2];
;             { const unsigned char* p = X1Q + (size_t)(nbase + tcur) * 2048u + (unsigned)lane * 16u; xq[0] = __builtin_nontemporal_load((const u4*)p); xq[1] = __builtin_nontemporal_load((const u4*)(p + 1024)); }
;             int lt = tnx, lts = (lt < 32) ? __builtin_amdgcn_readlane(gstv, lt) : 0x7fffffff;
;             float xs = __int_as_float(__builtin_amdgcn_readlane(__float_as_int(xsc_v), tcur));
;             int evn = 0; float wvn = 0.f;
;             if (lane < total) { evn = __builtin_nontemporal_load(FE + lane); wvn = __builtin_nontemporal_load(FW + lane); }
;     ...
;             int sx15; PU_SX();
.Lq_nnd1:
	s_mov_b32 s35, 0
	s_mov_b32 s50, s31
	s_mov_b32 s34, 0
	s_mov_b32 s11, 0
	s_cmp_gt_u32 s50, 31
	s_cbranch_scc1 .Lq_pp2
	v_readlane_b32 s4, v81, s50
	s_cmp_lg_u32 s4, 0
	s_cbranch_scc1 .Lq_pp2
	s_lshl_b32 s5, s50, 11
	s_add_u32 s6, s26, s5
	s_addc_u32 s7, s27, 0
	global_load_dwordx4 v[128:131], v206, s[6:7] nt
	global_load_dwordx4 v[132:135], v206, s[6:7] offset:1024 nt
	s_add_u32 s50, s50, 1

; #define PU_SX() do { int a_ = 0, b_ = 0; _Pragma("unroll") for (int q_ = 0; q_ < 4; ++q_) { a_ = __builtin_amdgcn_sdot4((int)xq[0][q_], 0x01010101, a_, false); b_ = __builtin_amdgcn_sdot4((int)xq[1][q_], 0x01010101, b_, false); } sx15 = 240 * a_ - 16 * b_; } while (0)
; __device__ __forceinline__ void phase_peer_bucket(const Params& P, unsigned char* ws, int l, LAS unsigned char* lds, int bid, int G, int lane, int wave) {
;     ...
;             int tcur = peer3_next_nonempty(gstv, 0); int tnx = peer3_next_nonempty(gstv, tcur + 1); int tend = __builtin_amdgcn_readlane(gstv, tcur + 1);
;             u4 xq[2];
;             { const unsigned char* p = X1Q + (size_t)(nbase + tcur) * 2048u + (unsigned)lane * 16u; xq[0] = __builtin_nontemporal_load((const u4*)p); xq[1] = __builtin_nontemporal_load((const u4*)(p + 1024)); }
;             int lt = tnx, lts = (lt < 32) ? __builtin_amdgcn_readlane(gstv, lt) : 0x7fffffff;
;             float xs = __int_as_float(__builtin_amdgcn_readlane(__float_as_int(xsc_v), tcur));
;             int evn = 0; float wvn = 0.f;
;             if (lane < total) { evn = __builtin_nontemporal_load(FE + lane); wvn = __builtin_nontemporal_load(FW + lane); }
;     ...
;             int sx15; PU_SX();
.Lq_nnd3:
	s_mov_b32 s56, -1
	s_cmp_gt_u32 s50, 31
	s_cbranch_scc1 .Lq_tr4
	v_readlane_b32 s56, v81, s50
	s_sub_u32 s56, s56, 16
.Lq_tr4:
.Lq_pp2:
	s_cmp_gt_u32 s50, 31
	s_cbranch_scc1 .Lq_pp5
	v_readlane_b32 s4, v81, s50
	s_cmp_lg_u32 s4, 4
	s_cbranch_scc1 .Lq_pp5
	s_lshl_b32 s5, s50, 11
	s_add_u32 s6, s26, s5
	s_addc_u32 s7, s27, 0
	global_load_dwordx4 v[136:139], v206, s[6:7] nt
	global_load_dwordx4 v[140:143], v206, s[6:7] offset:1024 nt
	s_add_u32 s50, s50, 1

.Lq_tr7:
.Lq_pp5:
	s_cmp_gt_u32 s50, 31
	s_cbranch_scc1 .Lq_pp8
	v_readlane_b32 s4, v81, s50
	s_cmp_lg_u32 s4, 8
	s_cbranch_scc1 .Lq_pp8
	s_lshl_b32 s5, s50, 11
	s_add_u32 s6, s26, s5
	s_addc_u32 s7, s27, 0
	global_load_dwordx4 v[144:147], v206, s[6:7] nt
	global_load_dwordx4 v[148:151], v206, s[6:7] offset:1024 nt
	s_add_u32 s50, s50, 1

.Lq_tr10:
.Lq_pp8:
	s_cmp_gt_u32 s50, 31
	s_cbranch_scc1 .Lq_pp11
	v_readlane_b32 s4, v81, s50
	s_cmp_lg_u32 s4, 12
	s_cbranch_scc1 .Lq_pp11
	s_lshl_b32 s5, s50, 11
	s_add_u32 s6, s26, s5
	s_addc_u32 s7, s27, 0
	global_load_dwordx4 v[152:155], v206, s[6:7] nt
	global_load_dwordx4 v[156:159], v206, s[6:7] offset:1024 nt
	s_add_u32 s50, s50, 1

; __device__ __forceinline__ int peer3_next_nonempty(int gstv, int t) {
;     while (t < 32 && __builtin_amdgcn_readlane(gstv, t + 1) == __builtin_amdgcn_readlane(gstv, t)) ++t;
;     return t;
.Lq_tr13:
.Lq_pp11:
	s_mov_b32 s56, -1
	s_cmp_gt_u32 s50, 31
	s_cbranch_scc1 .Lq_tr14
	v_readlane_b32 s56, v81, s50
	s_sub_u32 s56, s56, 16

; #define LAS __attribute__((address_space(3)))
; #define PU_DO(R, gi) do { PU_SWITCH(R, gi) peer3_dots(R, xq, sx15, red + lane * 68, (gi)); xsv = (lane >= PG * (gi) && lane < PG * (gi) + PG) ? xs : xsv; } while (0)
; __device__ __forceinline__ void peer3_dots(const u4 (&R)[PG][2], const u4 (&xq)[2], int sx15, LAS int* redrow, int g) {
;     static_assert(PG == 4, "one 16-byte LDS store per row group");
;     int d[4];
; #pragma unroll
;     for (int k = 0; k < 4; ++k) { int a = 0, ah = 0;
; #pragma unroll
;         for (int q = 0; q < 4; ++q) { const unsigned w = R[k][0][q];
;             a = __builtin_amdgcn_sdot4((int)(w & 0x0f0f0f0fu), (int)xq[0][q], a, false); ah = __builtin_amdgcn_sdot4((int)(w & 0xf0f0f0f0u), (int)xq[1][q], ah, false); }
;         d[k] = 32 * a + 2 * ah - sx15; }
;     u4 w; w.x = (unsigned)d[0]; w.y = (unsigned)d[1]; w.z = (unsigned)d[2]; w.w = (unsigned)d[3];
;     *(LAS u4*)(redrow + 4 * g) = w;
; }
; __device__ __forceinline__ void phase_peer_bucket(const Params& P, unsigned char* ws, int l, LAS unsigned char* lds, int bid, int G, int lane, int wave) {
;     ...
;             bool pre = false; u4 A[PG][2], B[PG][2], C[PG][2], Dq[PG][2];
; #pragma unroll 1
;             for (int blk = 0; blk < total; blk += 64) { const int blen = (total - blk) < 64 ? (total - blk) : 64, ng = blen / PG;
;                 const int ev = evn; const float wv = wvn;
;                 if (blk + 64 + lane < total) { evn = __builtin_nontemporal_load(FE + blk + 64 + lane); wvn = __builtin_nontemporal_load(FW + blk + 64 + lane); }
;                 const float us = USC[ev], vs = VSC[ev];
;                 float xsv = 0.f;
;                 if (ng == 16) {
;                     const bool nextfull = blk + 128 <= total;
;                     if (!pre) { PU_ROWS(A, 0); PU_ROWS(B, 1); PU_ROWS(C, 2); }
; #pragma unroll 1
;                     for (int g = 0; g < 12; g += 4) {
;                         PU_ROWS(Dq, g + 3); PU_DO(A, g); PU_ROWS(A, g + 4); PU_DO(B, g + 1); PU_ROWS(B, g + 5); PU_DO(C, g + 2); PU_ROWS(C, g + 6); PU_DO(Dq, g + 3);
;                     }
;                     PU_ROWS(Dq, 15); PU_DO(A, 12); if (nextfull) PU_ROWS_N(A, 0); PU_DO(B, 13); if (nextfull) PU_ROWS_N(B, 1); PU_DO(C, 14); if (nextfull) PU_ROWS_N(C, 2); PU_DO(Dq, 15);
.Lq_g0:
	s_add_u32 s11, s34, 0
	s_cmp_ge_u32 s11, s35
	s_cbranch_scc1 .Lq_sw0
.Lq_swret0:
	s_cmp_ge_u32 s11, s56
	s_cbranch_scc1 .Lq_stx0
.Lq_std0:
	s_waitcnt vmcnt(8)
	v_and_b32_e32 v96, 0xf0f0f0f, v0
	v_and_b32_e32 v100, 0xf0f0f0f0, v0
	v_and_b32_e32 v97, 0xf0f0f0f, v1
	v_and_b32_e32 v101, 0xf0f0f0f0, v1
	v_dot4_i32_i8 v104, v96, v64, 0
	v_dot4_i32_i8 v105, v100, v68, 0
	v_and_b32_e32 v98, 0xf0f0f0f, v2
	v_and_b32_e32 v102, 0xf0f0f0f0, v2
	v_dot4_i32_i8 v104, v97, v65, v104
	v_dot4_i32_i8 v105, v101, v69, v105
	v_and_b32_e32 v99, 0xf0f0f0f, v3
	v_and_b32_e32 v103, 0xf0f0f0f0, v3
	v_dot4_i32_i8 v104, v98, v66, v104
	v_dot4_i32_i8 v105, v102, v70, v105
	v_dot4_i32_i8 v104, v99, v67, v104
	v_dot4_i32_i8 v105, v103, v71, v105
	v_and_b32_e32 v96, 0xf0f0f0f, v4
	v_and_b32_e32 v100, 0xf0f0f0f0, v4
	v_and_b32_e32 v97, 0xf0f0f0f, v5
	v_and_b32_e32 v101, 0xf0f0f0f0, v5
	v_lshl_add_u32 v106, v104, 4, v105
	v_lshl_add_u32 v92, v106, 1, v72
	v_dot4_i32_i8 v126, v96, v64, 0
	v_dot4_i32_i8 v127, v100, v68, 0
	v_and_b32_e32 v98, 0xf0f0f0f, v6
	v_and_b32_e32 v102, 0xf0f0f0f0, v6
	v_dot4_i32_i8 v126, v97, v65, v126
	v_dot4_i32_i8 v127, v101, v69, v127
	v_and_b32_e32 v99, 0xf0f0f0f, v7
	v_and_b32_e32 v103, 0xf0f0f0f0, v7
	v_dot4_i32_i8 v126, v98, v66, v126
	v_dot4_i32_i8 v127, v102, v70, v127
	v_dot4_i32_i8 v126, v99, v67, v126
	v_dot4_i32_i8 v127, v103, v71, v127
	v_and_b32_e32 v96, 0xf0f0f0f, v8
	v_and_b32_e32 v100, 0xf0f0f0f0, v8
	v_and_b32_e32 v97, 0xf0f0f0f, v9
	v_and_b32_e32 v101, 0xf0f0f0f0, v9
	v_lshl_add_u32 v106, v126, 4, v127
	v_lshl_add_u32 v93, v106, 1, v72
	v_dot4_i32_i8 v104, v96, v64, 0
	v_dot4_i32_i8 v105, v100, v68, 0
	v_and_b32_e32 v98, 0xf0f0f0f, v10
	v_and_b32_e32 v102, 0xf0f0f0f0, v10
	v_dot4_i32_i8 v104, v97, v65, v104
	v_dot4_i32_i8 v105, v101, v69, v105
	v_and_b32_e32 v99, 0xf0f0f0f, v11
	v_and_b32_e32 v103, 0xf0f0f0f0, v11
	v_dot4_i32_i8 v104, v98, v66, v104
	v_dot4_i32_i8 v105, v102, v70, v105
	v_dot4_i32_i8 v104, v99, v67, v104
	v_dot4_i32_i8 v105, v103, v71, v105
	v_and_b32_e32 v96, 0xf0f0f0f, v12
	v_and_b32_e32 v100, 0xf0f0f0f0, v12
	v_and_b32_e32 v97, 0xf0f0f0f, v13
	v_and_b32_e32 v101, 0xf0f0f0f0, v13
	v_lshl_add_u32 v106, v104, 4, v105
	v_lshl_add_u32 v94, v106, 1, v72
	v_dot4_i32_i8 v126, v96, v64, 0
	v_dot4_i32_i8 v127, v100, v68, 0
	v_and_b32_e32 v98, 0xf0f0f0f, v14
	v_and_b32_e32 v102, 0xf0f0f0f0, v14
	v_dot4_i32_i8 v126, v97, v65, v126
	v_dot4_i32_i8 v127, v101, v69, v127
	v_and_b32_e32 v99, 0xf0f0f0f, v15
	v_and_b32_e32 v103, 0xf0f0f0f0, v15
	v_dot4_i32_i8 v126, v98, v66, v126
	v_dot4_i32_i8 v127, v102, v70, v127
	v_dot4_i32_i8 v126, v99, v67, v126
	v_dot4_i32_i8 v127, v103, v71, v127
	s_nop 0
	v_readlane_b32 s36, v75, 12
	v_readlane_b32 s5, v75, 13
	v_readlane_b32 s6, v75, 14
	v_readlane_b32 s7, v75, 15
	v_lshl_add_u32 v106, v126, 4, v127
	v_lshl_add_u32 v95, v106, 1, v72
	v_add_u32_e32 v113, s36, v206
	v_add_u32_e32 v114, s5, v206
	v_add_u32_e32 v115, s6, v206
	v_add_u32_e32 v116, s7, v206
	global_load_dwordx4 v[48:51], v113, s[52:53]
	global_load_dwordx4 v[52:55], v114, s[52:53]
	global_load_dwordx4 v[56:59], v115, s[52:53]
	global_load_dwordx4 v[60:63], v116, s[52:53]
	ds_write_b128 v107, v[92:95] offset:0
	s_mov_b64 exec, s[22:23]
	v_mov_b32_e32 v87, s10
	s_mov_b64 exec, -1
.Lq_g1:
	s_add_u32 s11, s34, 4
	s_cmp_ge_u32 s11, s35
	s_cbranch_scc1 .Lq_sw1

; #define LAS __attribute__((address_space(3)))
; #define PU_DO(R, gi) do { PU_SWITCH(R, gi) peer3_dots(R, xq, sx15, red + lane * 68, (gi)); xsv = (lane >= PG * (gi) && lane < PG * (gi) + PG) ? xs : xsv; } while (0)
; __device__ __forceinline__ void peer3_dots(const u4 (&R)[PG][2], const u4 (&xq)[2], int sx15, LAS int* redrow, int g) {
;     static_assert(PG == 4, "one 16-byte LDS store per row group");
;     int d[4];
; #pragma unroll
;     for (int k = 0; k < 4; ++k) { int a = 0, ah = 0;
; #pragma unroll
;         for (int q = 0; q < 4; ++q) { const unsigned w = R[k][0][q];
;             a = __builtin_amdgcn_sdot4((int)(w & 0x0f0f0f0fu), (int)xq[0][q], a, false); ah = __builtin_amdgcn_sdot4((int)(w & 0xf0f0f0f0u), (int)xq[1][q], ah, false); }
;         d[k] = 32 * a + 2 * ah - sx15; }
;     u4 w; w.x = (unsigned)d[0]; w.y = (unsigned)d[1]; w.z = (unsigned)d[2]; w.w = (unsigned)d[3];
;     *(LAS u4*)(redrow + 4 * g) = w;
; }
; __device__ __forceinline__ void phase_peer_bucket(const Params& P, unsigned char* ws, int l, LAS unsigned char* lds, int bid, int G, int lane, int wave) {
;     ...
;             bool pre = false; u4 A[PG][2], B[PG][2], C[PG][2], Dq[PG][2];
; #pragma unroll 1
;             for (int blk = 0; blk < total; blk += 64) { const int blen = (total - blk) < 64 ? (total - blk) : 64, ng = blen / PG;
;                 const int ev = evn; const float wv = wvn;
;                 if (blk + 64 + lane < total) { evn = __builtin_nontemporal_load(FE + blk + 64 + lane); wvn = __builtin_nontemporal_load(FW + blk + 64 + lane); }
;                 const float us = USC[ev], vs = VSC[ev];
;                 float xsv = 0.f;
;                 if (ng == 16) {
;                     const bool nextfull = blk + 128 <= total;
;                     if (!pre) { PU_ROWS(A, 0); PU_ROWS(B, 1); PU_ROWS(C, 2); }
; #pragma unroll 1
;                     for (int g = 0; g < 12; g += 4) {
;                         PU_ROWS(Dq, g + 3); PU_DO(A, g); PU_ROWS(A, g + 4); PU_DO(B, g + 1); PU_ROWS(B, g + 5); PU_DO(C, g + 2); PU_ROWS(C, g + 6); PU_DO(Dq, g + 3);
;                     }
;                     PU_ROWS(Dq, 15); PU_DO(A, 12); if (nextfull) PU_ROWS_N(A, 0); PU_DO(B, 13); if (nextfull) PU_ROWS_N(B, 1); PU_DO(C, 14); if (nextfull) PU_ROWS_N(C, 2); PU_DO(Dq, 15);
.Lq_std1:
	s_waitcnt vmcnt(8)
	v_and_b32_e32 v96, 0xf0f0f0f, v16
	v_and_b32_e32 v100, 0xf0f0f0f0, v16
	v_and_b32_e32 v97, 0xf0f0f0f, v17
	v_and_b32_e32 v101, 0xf0f0f0f0, v17
	v_dot4_i32_i8 v104, v96, v64, 0
	v_dot4_i32_i8 v105, v100, v68, 0
	v_and_b32_e32 v98, 0xf0f0f0f, v18
	v_and_b32_e32 v102, 0xf0f0f0f0, v18
	v_dot4_i32_i8 v104, v97, v65, v104
	v_dot4_i32_i8 v105, v101, v69, v105
	v_and_b32_e32 v99, 0xf0f0f0f, v19
	v_and_b32_e32 v103, 0xf0f0f0f0, v19
	v_dot4_i32_i8 v104, v98, v66, v104
	v_dot4_i32_i8 v105, v102, v70, v105
	v_dot4_i32_i8 v104, v99, v67, v104
	v_dot4_i32_i8 v105, v103, v71, v105
	v_and_b32_e32 v96, 0xf0f0f0f, v20
	v_and_b32_e32 v100, 0xf0f0f0f0, v20
	v_and_b32_e32 v97, 0xf0f0f0f, v21
	v_and_b32_e32 v101, 0xf0f0f0f0, v21
	v_lshl_add_u32 v106, v104, 4, v105
	v_lshl_add_u32 v92, v106, 1, v72
	v_dot4_i32_i8 v126, v96, v64, 0
	v_dot4_i32_i8 v127, v100, v68, 0
	v_and_b32_e32 v98, 0xf0f0f0f, v22
	v_and_b32_e32 v102, 0xf0f0f0f0, v22
	v_dot4_i32_i8 v126, v97, v65, v126
	v_dot4_i32_i8 v127, v101, v69, v127
	v_and_b32_e32 v99, 0xf0f0f0f, v23
	v_and_b32_e32 v103, 0xf0f0f0f0, v23
	v_dot4_i32_i8 v126, v98, v66, v126
	v_dot4_i32_i8 v127, v102, v70, v127
	v_dot4_i32_i8 v126, v99, v67, v126
	v_dot4_i32_i8 v127, v103, v71, v127
	v_and_b32_e32 v96, 0xf0f0f0f, v24
	v_and_b32_e32 v100, 0xf0f0f0f0, v24
	v_and_b32_e32 v97, 0xf0f0f0f, v25
	v_and_b32_e32 v101, 0xf0f0f0f0, v25
	v_lshl_add_u32 v106, v126, 4, v127
	v_lshl_add_u32 v93, v106, 1, v72
	v_dot4_i32_i8 v104, v96, v64, 0
	v_dot4_i32_i8 v105, v100, v68, 0
	v_and_b32_e32 v98, 0xf0f0f0f, v26
	v_and_b32_e32 v102, 0xf0f0f0f0, v26
	v_dot4_i32_i8 v104, v97, v65, v104
	v_dot4_i32_i8 v105, v101, v69, v105
	v_and_b32_e32 v99, 0xf0f0f0f, v27
	v_and_b32_e32 v103, 0xf0f0f0f0, v27
	v_dot4_i32_i8 v104, v98, v66, v104
	v_dot4_i32_i8 v105, v102, v70, v105
	v_dot4_i32_i8 v104, v99, v67, v104
	v_dot4_i32_i8 v105, v103, v71, v105
	v_and_b32_e32 v96, 0xf0f0f0f, v28
	v_and_b32_e32 v100, 0xf0f0f0f0, v28
	v_and_b32_e32 v97, 0xf0f0f0f, v29
	v_and_b32_e32 v101, 0xf0f0f0f0, v29
	v_lshl_add_u32 v106, v104, 4, v105
	v_lshl_add_u32 v94, v106, 1, v72
	v_dot4_i32_i8 v126, v96, v64, 0
	v_dot4_i32_i8 v127, v100, v68, 0
	v_and_b32_e32 v98, 0xf0f0f0f, v30
	v_and_b32_e32 v102, 0xf0f0f0f0, v30
	v_dot4_i32_i8 v126, v97, v65, v126
	v_dot4_i32_i8 v127, v101, v69, v127
	v_and_b32_e32 v99, 0xf0f0f0f, v31
	v_and_b32_e32 v103, 0xf0f0f0f0, v31
	v_dot4_i32_i8 v126, v98, v66, v126
	v_dot4_i32_i8 v127, v102, v70, v127
	v_dot4_i32_i8 v126, v99, v67, v126
	v_dot4_i32_i8 v127, v103, v71, v127
	s_nop 0
	v_readlane_b32 s36, v75, 16
	v_readlane_b32 s5, v75, 17
	v_readlane_b32 s6, v75, 18
	v_readlane_b32 s7, v75, 19
	v_lshl_add_u32 v106, v126, 4, v127
	v_lshl_add_u32 v95, v106, 1, v72
	v_add_u32_e32 v113, s36, v206
	v_add_u32_e32 v114, s5, v206
	v_add_u32_e32 v115, s6, v206
	v_add_u32_e32 v116, s7, v206
	global_load_dwordx4 v[0:3], v113, s[52:53]
	global_load_dwordx4 v[4:7], v114, s[52:53]
	global_load_dwordx4 v[8:11], v115, s[52:53]
	global_load_dwordx4 v[12:15], v116, s[52:53]
	ds_write_b128 v107, v[92:95] offset:16
	s_lshl_b64 exec, s[22:23], 4
	v_mov_b32_e32 v87, s10
	s_mov_b64 exec, -1
.Lq_g2:
	s_add_u32 s11, s34, 8
	s_cmp_ge_u32 s11, s35
	s_cbranch_scc1 .Lq_sw2

; #define LAS __attribute__((address_space(3)))
; #define PU_DO(R, gi) do { PU_SWITCH(R, gi) peer3_dots(R, xq, sx15, red + lane * 68, (gi)); xsv = (lane >= PG * (gi) && lane < PG * (gi) + PG) ? xs : xsv; } while (0)
; __device__ __forceinline__ void peer3_dots(const u4 (&R)[PG][2], const u4 (&xq)[2], int sx15, LAS int* redrow, int g) {
;     static_assert(PG == 4, "one 16-byte LDS store per row group");
;     int d[4];
; #pragma unroll
;     for (int k = 0; k < 4; ++k) { int a = 0, ah = 0;
; #pragma unroll
;         for (int q = 0; q < 4; ++q) { const unsigned w = R[k][0][q];
;             a = __builtin_amdgcn_sdot4((int)(w & 0x0f0f0f0fu), (int)xq[0][q], a, false); ah = __builtin_amdgcn_sdot4((int)(w & 0xf0f0f0f0u), (int)xq[1][q], ah, false); }
;         d[k] = 32 * a + 2 * ah - sx15; }
;     u4 w; w.x = (unsigned)d[0]; w.y = (unsigned)d[1]; w.z = (unsigned)d[2]; w.w = (unsigned)d[3];
;     *(LAS u4*)(redrow + 4 * g) = w;
; }
; __device__ __forceinline__ void phase_peer_bucket(const Params& P, unsigned char* ws, int l, LAS unsigned char* lds, int bid, int G, int lane, int wave) {
;     ...
;             bool pre = false; u4 A[PG][2], B[PG][2], C[PG][2], Dq[PG][2];
; #pragma unroll 1
;             for (int blk = 0; blk < total; blk += 64) { const int blen = (total - blk) < 64 ? (total - blk) : 64, ng = blen / PG;
;                 const int ev = evn; const float wv = wvn;
;                 if (blk + 64 + lane < total) { evn = __builtin_nontemporal_load(FE + blk + 64 + lane); wvn = __builtin_nontemporal_load(FW + blk + 64 + lane); }
;                 const float us = USC[ev], vs = VSC[ev];
;                 float xsv = 0.f;
;                 if (ng == 16) {
;                     const bool nextfull = blk + 128 <= total;
;                     if (!pre) { PU_ROWS(A, 0); PU_ROWS(B, 1); PU_ROWS(C, 2); }
; #pragma unroll 1
;                     for (int g = 0; g < 12; g += 4) {
;                         PU_ROWS(Dq, g + 3); PU_DO(A, g); PU_ROWS(A, g + 4); PU_DO(B, g + 1); PU_ROWS(B, g + 5); PU_DO(C, g + 2); PU_ROWS(C, g + 6); PU_DO(Dq, g + 3);
;                     }
;                     PU_ROWS(Dq, 15); PU_DO(A, 12); if (nextfull) PU_ROWS_N(A, 0); PU_DO(B, 13); if (nextfull) PU_ROWS_N(B, 1); PU_DO(C, 14); if (nextfull) PU_ROWS_N(C, 2); PU_DO(Dq, 15);
.Lq_std2:
	s_waitcnt vmcnt(8)
	v_and_b32_e32 v96, 0xf0f0f0f, v32
	v_and_b32_e32 v100, 0xf0f0f0f0, v32
	v_and_b32_e32 v97, 0xf0f0f0f, v33
	v_and_b32_e32 v101, 0xf0f0f0f0, v33
	v_dot4_i32_i8 v104, v96, v64, 0
	v_dot4_i32_i8 v105, v100, v68, 0
	v_and_b32_e32 v98, 0xf0f0f0f, v34
	v_and_b32_e32 v102, 0xf0f0f0f0, v34
	v_dot4_i32_i8 v104, v97, v65, v104
	v_dot4_i32_i8 v105, v101, v69, v105
	v_and_b32_e32 v99, 0xf0f0f0f, v35
	v_and_b32_e32 v103, 0xf0f0f0f0, v35
	v_dot4_i32_i8 v104, v98, v66, v104
	v_dot4_i32_i8 v105, v102, v70, v105
	v_dot4_i32_i8 v104, v99, v67, v104
	v_dot4_i32_i8 v105, v103, v71, v105
	v_and_b32_e32 v96, 0xf0f0f0f, v36
	v_and_b32_e32 v100, 0xf0f0f0f0, v36
	v_and_b32_e32 v97, 0xf0f0f0f, v37
	v_and_b32_e32 v101, 0xf0f0f0f0, v37
	v_lshl_add_u32 v106, v104, 4, v105
	v_lshl_add_u32 v92, v106, 1, v72
	v_dot4_i32_i8 v126, v96, v64, 0
	v_dot4_i32_i8 v127, v100, v68, 0
	v_and_b32_e32 v98, 0xf0f0f0f, v38
	v_and_b32_e32 v102, 0xf0f0f0f0, v38
	v_dot4_i32_i8 v126, v97, v65, v126
	v_dot4_i32_i8 v127, v101, v69, v127
	v_and_b32_e32 v99, 0xf0f0f0f, v39
	v_and_b32_e32 v103, 0xf0f0f0f0, v39
	v_dot4_i32_i8 v126, v98, v66, v126
	v_dot4_i32_i8 v127, v102, v70, v127
	v_dot4_i32_i8 v126, v99, v67, v126
	v_dot4_i32_i8 v127, v103, v71, v127
	v_and_b32_e32 v96, 0xf0f0f0f, v40
	v_and_b32_e32 v100, 0xf0f0f0f0, v40
	v_and_b32_e32 v97, 0xf0f0f0f, v41
	v_and_b32_e32 v101, 0xf0f0f0f0, v41
	v_lshl_add_u32 v106, v126, 4, v127
	v_lshl_add_u32 v93, v106, 1, v72
	v_dot4_i32_i8 v104, v96, v64, 0
	v_dot4_i32_i8 v105, v100, v68, 0
	v_and_b32_e32 v98, 0xf0f0f0f, v42
	v_and_b32_e32 v102, 0xf0f0f0f0, v42
	v_dot4_i32_i8 v104, v97, v65, v104
	v_dot4_i32_i8 v105, v101, v69, v105
	v_and_b32_e32 v99, 0xf0f0f0f, v43
	v_and_b32_e32 v103, 0xf0f0f0f0, v43
	v_dot4_i32_i8 v104, v98, v66, v104
	v_dot4_i32_i8 v105, v102, v70, v105
	v_dot4_i32_i8 v104, v99, v67, v104
	v_dot4_i32_i8 v105, v103, v71, v105
	v_and_b32_e32 v96, 0xf0f0f0f, v44
	v_and_b32_e32 v100, 0xf0f0f0f0, v44
	v_and_b32_e32 v97, 0xf0f0f0f, v45
	v_and_b32_e32 v101, 0xf0f0f0f0, v45
	v_lshl_add_u32 v106, v104, 4, v105
	v_lshl_add_u32 v94, v106, 1, v72
	v_dot4_i32_i8 v126, v96, v64, 0
	v_dot4_i32_i8 v127, v100, v68, 0
	v_and_b32_e32 v98, 0xf0f0f0f, v46
	v_and_b32_e32 v102, 0xf0f0f0f0, v46
	v_dot4_i32_i8 v126, v97, v65, v126
	v_dot4_i32_i8 v127, v101, v69, v127
	v_and_b32_e32 v99, 0xf0f0f0f, v47
	v_and_b32_e32 v103, 0xf0f0f0f0, v47
	v_dot4_i32_i8 v126, v98, v66, v126
	v_dot4_i32_i8 v127, v102, v70, v127
	v_dot4_i32_i8 v126, v99, v67, v126
	v_dot4_i32_i8 v127, v103, v71, v127
	s_nop 0
	v_readlane_b32 s36, v75, 20
	v_readlane_b32 s5, v75, 21
	v_readlane_b32 s6, v75, 22
	v_readlane_b32 s7, v75, 23
	v_lshl_add_u32 v106, v126, 4, v127
	v_lshl_add_u32 v95, v106, 1, v72
	v_add_u32_e32 v113, s36, v206
	v_add_u32_e32 v114, s5, v206
	v_add_u32_e32 v115, s6, v206
	v_add_u32_e32 v116, s7, v206
	global_load_dwordx4 v[16:19], v113, s[52:53]
	global_load_dwordx4 v[20:23], v114, s[52:53]
	global_load_dwordx4 v[24:27], v115, s[52:53]
	global_load_dwordx4 v[28:31], v116, s[52:53]
	ds_write_b128 v107, v[92:95] offset:32
	s_lshl_b64 exec, s[22:23], 8
	v_mov_b32_e32 v87, s10
	s_mov_b64 exec, -1
.Lq_g3:
	s_add_u32 s11, s34, 12
	s_cmp_ge_u32 s11, s35
	s_cbranch_scc1 .Lq_sw3

; #define LAS __attribute__((address_space(3)))
; #define PU_DO(R, gi) do { PU_SWITCH(R, gi) peer3_dots(R, xq, sx15, red + lane * 68, (gi)); xsv = (lane >= PG * (gi) && lane < PG * (gi) + PG) ? xs : xsv; } while (0)
; __device__ __forceinline__ void peer3_dots(const u4 (&R)[PG][2], const u4 (&xq)[2], int sx15, LAS int* redrow, int g) {
;     static_assert(PG == 4, "one 16-byte LDS store per row group");
;     int d[4];
; #pragma unroll
;     for (int k = 0; k < 4; ++k) { int a = 0, ah = 0;
; #pragma unroll
;         for (int q = 0; q < 4; ++q) { const unsigned w = R[k][0][q];
;             a = __builtin_amdgcn_sdot4((int)(w & 0x0f0f0f0fu), (int)xq[0][q], a, false); ah = __builtin_amdgcn_sdot4((int)(w & 0xf0f0f0f0u), (int)xq[1][q], ah, false); }
;         d[k] = 32 * a + 2 * ah - sx15; }
;     u4 w; w.x = (unsigned)d[0]; w.y = (unsigned)d[1]; w.z = (unsigned)d[2]; w.w = (unsigned)d[3];
;     *(LAS u4*)(redrow + 4 * g) = w;
; }
; __device__ __forceinline__ void phase_peer_bucket(const Params& P, unsigned char* ws, int l, LAS unsigned char* lds, int bid, int G, int lane, int wave) {
;     ...
;             bool pre = false; u4 A[PG][2], B[PG][2], C[PG][2], Dq[PG][2];
; #pragma unroll 1
;             for (int blk = 0; blk < total; blk += 64) { const int blen = (total - blk) < 64 ? (total - blk) : 64, ng = blen / PG;
;                 const int ev = evn; const float wv = wvn;
;                 if (blk + 64 + lane < total) { evn = __builtin_nontemporal_load(FE + blk + 64 + lane); wvn = __builtin_nontemporal_load(FW + blk + 64 + lane); }
;                 const float us = USC[ev], vs = VSC[ev];
;                 float xsv = 0.f;
;                 if (ng == 16) {
;                     const bool nextfull = blk + 128 <= total;
;                     if (!pre) { PU_ROWS(A, 0); PU_ROWS(B, 1); PU_ROWS(C, 2); }
; #pragma unroll 1
;                     for (int g = 0; g < 12; g += 4) {
;                         PU_ROWS(Dq, g + 3); PU_DO(A, g); PU_ROWS(A, g + 4); PU_DO(B, g + 1); PU_ROWS(B, g + 5); PU_DO(C, g + 2); PU_ROWS(C, g + 6); PU_DO(Dq, g + 3);
;                     }
;                     PU_ROWS(Dq, 15); PU_DO(A, 12); if (nextfull) PU_ROWS_N(A, 0); PU_DO(B, 13); if (nextfull) PU_ROWS_N(B, 1); PU_DO(C, 14); if (nextfull) PU_ROWS_N(C, 2); PU_DO(Dq, 15);
.Lq_std3:
	s_waitcnt vmcnt(8)
	v_and_b32_e32 v96, 0xf0f0f0f, v48
	v_and_b32_e32 v100, 0xf0f0f0f0, v48
	v_and_b32_e32 v97, 0xf0f0f0f, v49
	v_and_b32_e32 v101, 0xf0f0f0f0, v49
	v_dot4_i32_i8 v104, v96, v64, 0
	v_dot4_i32_i8 v105, v100, v68, 0
	v_and_b32_e32 v98, 0xf0f0f0f, v50
	v_and_b32_e32 v102, 0xf0f0f0f0, v50
	v_dot4_i32_i8 v104, v97, v65, v104
	v_dot4_i32_i8 v105, v101, v69, v105
	v_and_b32_e32 v99, 0xf0f0f0f, v51
	v_and_b32_e32 v103, 0xf0f0f0f0, v51
	v_dot4_i32_i8 v104, v98, v66, v104
	v_dot4_i32_i8 v105, v102, v70, v105
	v_dot4_i32_i8 v104, v99, v67, v104
	v_dot4_i32_i8 v105, v103, v71, v105
	v_and_b32_e32 v96, 0xf0f0f0f, v52
	v_and_b32_e32 v100, 0xf0f0f0f0, v52
	v_and_b32_e32 v97, 0xf0f0f0f, v53
	v_and_b32_e32 v101, 0xf0f0f0f0, v53
	v_lshl_add_u32 v106, v104, 4, v105
	v_lshl_add_u32 v92, v106, 1, v72
	v_dot4_i32_i8 v126, v96, v64, 0
	v_dot4_i32_i8 v127, v100, v68, 0
	v_and_b32_e32 v98, 0xf0f0f0f, v54
	v_and_b32_e32 v102, 0xf0f0f0f0, v54
	v_dot4_i32_i8 v126, v97, v65, v126
	v_dot4_i32_i8 v127, v101, v69, v127
	v_and_b32_e32 v99, 0xf0f0f0f, v55
	v_and_b32_e32 v103, 0xf0f0f0f0, v55
	v_dot4_i32_i8 v126, v98, v66, v126
	v_dot4_i32_i8 v127, v102, v70, v127
	v_dot4_i32_i8 v126, v99, v67, v126
	v_dot4_i32_i8 v127, v103, v71, v127
	v_and_b32_e32 v96, 0xf0f0f0f, v56
	v_and_b32_e32 v100, 0xf0f0f0f0, v56
	v_and_b32_e32 v97, 0xf0f0f0f, v57
	v_and_b32_e32 v101, 0xf0f0f0f0, v57
	v_lshl_add_u32 v106, v126, 4, v127
	v_lshl_add_u32 v93, v106, 1, v72
	v_dot4_i32_i8 v104, v96, v64, 0
	v_dot4_i32_i8 v105, v100, v68, 0
	v_and_b32_e32 v98, 0xf0f0f0f, v58
	v_and_b32_e32 v102, 0xf0f0f0f0, v58
	v_dot4_i32_i8 v104, v97, v65, v104
	v_dot4_i32_i8 v105, v101, v69, v105
	v_and_b32_e32 v99, 0xf0f0f0f, v59
	v_and_b32_e32 v103, 0xf0f0f0f0, v59
	v_dot4_i32_i8 v104, v98, v66, v104
	v_dot4_i32_i8 v105, v102, v70, v105
	v_dot4_i32_i8 v104, v99, v67, v104
	v_dot4_i32_i8 v105, v103, v71, v105
	v_and_b32_e32 v96, 0xf0f0f0f, v60
	v_and_b32_e32 v100, 0xf0f0f0f0, v60
	v_and_b32_e32 v97, 0xf0f0f0f, v61
	v_and_b32_e32 v101, 0xf0f0f0f0, v61
	v_lshl_add_u32 v106, v104, 4, v105
	v_lshl_add_u32 v94, v106, 1, v72
	v_dot4_i32_i8 v126, v96, v64, 0
	v_dot4_i32_i8 v127, v100, v68, 0
	v_and_b32_e32 v98, 0xf0f0f0f, v62
	v_and_b32_e32 v102, 0xf0f0f0f0, v62
	v_dot4_i32_i8 v126, v97, v65, v126
	v_dot4_i32_i8 v127, v101, v69, v127
	v_and_b32_e32 v99, 0xf0f0f0f, v63
	v_and_b32_e32 v103, 0xf0f0f0f0, v63
	v_dot4_i32_i8 v126, v98, v66, v126
	v_dot4_i32_i8 v127, v102, v70, v127
	v_dot4_i32_i8 v126, v99, v67, v126
	v_dot4_i32_i8 v127, v103, v71, v127
	s_nop 0
	v_readlane_b32 s36, v75, 24
	v_readlane_b32 s5, v75, 25
	v_readlane_b32 s6, v75, 26
	v_readlane_b32 s7, v75, 27
	v_lshl_add_u32 v106, v126, 4, v127
	v_lshl_add_u32 v95, v106, 1, v72
	v_add_u32_e32 v113, s36, v206
	v_add_u32_e32 v114, s5, v206
	v_add_u32_e32 v115, s6, v206
	v_add_u32_e32 v116, s7, v206
	global_load_dwordx4 v[32:35], v113, s[52:53]
	global_load_dwordx4 v[36:39], v114, s[52:53]
	global_load_dwordx4 v[40:43], v115, s[52:53]
	global_load_dwordx4 v[44:47], v116, s[52:53]
	ds_write_b128 v107, v[92:95] offset:48
	s_lshl_b64 exec, s[22:23], 12
	v_mov_b32_e32 v87, s10
	s_mov_b64 exec, -1
.Lq_g4:
	s_add_u32 s11, s34, 16
	s_cmp_ge_u32 s11, s35
	s_cbranch_scc1 .Lq_sw4

; #define LAS __attribute__((address_space(3)))
; #define PU_DO(R, gi) do { PU_SWITCH(R, gi) peer3_dots(R, xq, sx15, red + lane * 68, (gi)); xsv = (lane >= PG * (gi) && lane < PG * (gi) + PG) ? xs : xsv; } while (0)
; __device__ __forceinline__ void peer3_dots(const u4 (&R)[PG][2], const u4 (&xq)[2], int sx15, LAS int* redrow, int g) {
;     static_assert(PG == 4, "one 16-byte LDS store per row group");
;     int d[4];
; #pragma unroll
;     for (int k = 0; k < 4; ++k) { int a = 0, ah = 0;
; #pragma unroll
;         for (int q = 0; q < 4; ++q) { const unsigned w = R[k][0][q];
;             a = __builtin_amdgcn_sdot4((int)(w & 0x0f0f0f0fu), (int)xq[0][q], a, false); ah = __builtin_amdgcn_sdot4((int)(w & 0xf0f0f0f0u), (int)xq[1][q], ah, false); }
;         d[k] = 32 * a + 2 * ah - sx15; }
;     u4 w; w.x = (unsigned)d[0]; w.y = (unsigned)d[1]; w.z = (unsigned)d[2]; w.w = (unsigned)d[3];
;     *(LAS u4*)(redrow + 4 * g) = w;
; }
; __device__ __forceinline__ void phase_peer_bucket(const Params& P, unsigned char* ws, int l, LAS unsigned char* lds, int bid, int G, int lane, int wave) {
;     ...
;             bool pre = false; u4 A[PG][2], B[PG][2], C[PG][2], Dq[PG][2];
; #pragma unroll 1
;             for (int blk = 0; blk < total; blk += 64) { const int blen = (total - blk) < 64 ? (total - blk) : 64, ng = blen / PG;
;                 const int ev = evn; const float wv = wvn;
;                 if (blk + 64 + lane < total) { evn = __builtin_nontemporal_load(FE + blk + 64 + lane); wvn = __builtin_nontemporal_load(FW + blk + 64 + lane); }
;                 const float us = USC[ev], vs = VSC[ev];
;                 float xsv = 0.f;
;                 if (ng == 16) {
;                     const bool nextfull = blk + 128 <= total;
;                     if (!pre) { PU_ROWS(A, 0); PU_ROWS(B, 1); PU_ROWS(C, 2); }
; #pragma unroll 1
;                     for (int g = 0; g < 12; g += 4) {
;                         PU_ROWS(Dq, g + 3); PU_DO(A, g); PU_ROWS(A, g + 4); PU_DO(B, g + 1); PU_ROWS(B, g + 5); PU_DO(C, g + 2); PU_ROWS(C, g + 6); PU_DO(Dq, g + 3);
;                     }
;                     PU_ROWS(Dq, 15); PU_DO(A, 12); if (nextfull) PU_ROWS_N(A, 0); PU_DO(B, 13); if (nextfull) PU_ROWS_N(B, 1); PU_DO(C, 14); if (nextfull) PU_ROWS_N(C, 2); PU_DO(Dq, 15);
.Lq_std4:
	s_waitcnt vmcnt(8)
	v_and_b32_e32 v96, 0xf0f0f0f, v0
	v_and_b32_e32 v100, 0xf0f0f0f0, v0
	v_and_b32_e32 v97, 0xf0f0f0f, v1
	v_and_b32_e32 v101, 0xf0f0f0f0, v1
	v_dot4_i32_i8 v104, v96, v64, 0
	v_dot4_i32_i8 v105, v100, v68, 0
	v_and_b32_e32 v98, 0xf0f0f0f, v2
	v_and_b32_e32 v102, 0xf0f0f0f0, v2
	v_dot4_i32_i8 v104, v97, v65, v104
	v_dot4_i32_i8 v105, v101, v69, v105
	v_and_b32_e32 v99, 0xf0f0f0f, v3
	v_and_b32_e32 v103, 0xf0f0f0f0, v3
	v_dot4_i32_i8 v104, v98, v66, v104
	v_dot4_i32_i8 v105, v102, v70, v105
	v_dot4_i32_i8 v104, v99, v67, v104
	v_dot4_i32_i8 v105, v103, v71, v105
	v_and_b32_e32 v96, 0xf0f0f0f, v4
	v_and_b32_e32 v100, 0xf0f0f0f0, v4
	v_and_b32_e32 v97, 0xf0f0f0f, v5
	v_and_b32_e32 v101, 0xf0f0f0f0, v5
	v_lshl_add_u32 v106, v104, 4, v105
	v_lshl_add_u32 v92, v106, 1, v72
	v_dot4_i32_i8 v126, v96, v64, 0
	v_dot4_i32_i8 v127, v100, v68, 0
	v_and_b32_e32 v98, 0xf0f0f0f, v6
	v_and_b32_e32 v102, 0xf0f0f0f0, v6
	v_dot4_i32_i8 v126, v97, v65, v126
	v_dot4_i32_i8 v127, v101, v69, v127
	v_and_b32_e32 v99, 0xf0f0f0f, v7
	v_and_b32_e32 v103, 0xf0f0f0f0, v7
	v_dot4_i32_i8 v126, v98, v66, v126
	v_dot4_i32_i8 v127, v102, v70, v127
	v_dot4_i32_i8 v126, v99, v67, v126
	v_dot4_i32_i8 v127, v103, v71, v127
	v_and_b32_e32 v96, 0xf0f0f0f, v8
	v_and_b32_e32 v100, 0xf0f0f0f0, v8
	v_and_b32_e32 v97, 0xf0f0f0f, v9
	v_and_b32_e32 v101, 0xf0f0f0f0, v9
	v_lshl_add_u32 v106, v126, 4, v127
	v_lshl_add_u32 v93, v106, 1, v72
	v_dot4_i32_i8 v104, v96, v64, 0
	v_dot4_i32_i8 v105, v100, v68, 0
	v_and_b32_e32 v98, 0xf0f0f0f, v10
	v_and_b32_e32 v102, 0xf0f0f0f0, v10
	v_dot4_i32_i8 v104, v97, v65, v104
	v_dot4_i32_i8 v105, v101, v69, v105
	v_and_b32_e32 v99, 0xf0f0f0f, v11
	v_and_b32_e32 v103, 0xf0f0f0f0, v11
	v_dot4_i32_i8 v104, v98, v66, v104
	v_dot4_i32_i8 v105, v102, v70, v105
	v_dot4_i32_i8 v104, v99, v67, v104
	v_dot4_i32_i8 v105, v103, v71, v105
	v_and_b32_e32 v96, 0xf0f0f0f, v12
	v_and_b32_e32 v100, 0xf0f0f0f0, v12
	v_and_b32_e32 v97, 0xf0f0f0f, v13
	v_and_b32_e32 v101, 0xf0f0f0f0, v13
	v_lshl_add_u32 v106, v104, 4, v105
	v_lshl_add_u32 v94, v106, 1, v72
	v_dot4_i32_i8 v126, v96, v64, 0
	v_dot4_i32_i8 v127, v100, v68, 0
	v_and_b32_e32 v98, 0xf0f0f0f, v14
	v_and_b32_e32 v102, 0xf0f0f0f0, v14
	v_dot4_i32_i8 v126, v97, v65, v126
	v_dot4_i32_i8 v127, v101, v69, v127
	v_and_b32_e32 v99, 0xf0f0f0f, v15
	v_and_b32_e32 v103, 0xf0f0f0f0, v15
	v_dot4_i32_i8 v126, v98, v66, v126
	v_dot4_i32_i8 v127, v102, v70, v127
	v_dot4_i32_i8 v126, v99, v67, v126
	v_dot4_i32_i8 v127, v103, v71, v127
	s_nop 0
	v_readlane_b32 s36, v75, 28
	v_readlane_b32 s5, v75, 29
	v_readlane_b32 s6, v75, 30
	v_readlane_b32 s7, v75, 31
	v_lshl_add_u32 v106, v126, 4, v127
	v_lshl_add_u32 v95, v106, 1, v72
	v_add_u32_e32 v113, s36, v206
	v_add_u32_e32 v114, s5, v206
	v_add_u32_e32 v115, s6, v206
	v_add_u32_e32 v116, s7, v206
	global_load_dwordx4 v[48:51], v113, s[52:53]
	global_load_dwordx4 v[52:55], v114, s[52:53]
	global_load_dwordx4 v[56:59], v115, s[52:53]
	global_load_dwordx4 v[60:63], v116, s[52:53]
	ds_write_b128 v107, v[92:95] offset:64
	s_lshl_b64 exec, s[22:23], 16
	v_mov_b32_e32 v87, s10
	s_mov_b64 exec, -1
.Lq_g5:
	s_add_u32 s11, s34, 20
	s_cmp_ge_u32 s11, s35
	s_cbranch_scc1 .Lq_sw5

; #define LAS __attribute__((address_space(3)))
; #define PU_DO(R, gi) do { PU_SWITCH(R, gi) peer3_dots(R, xq, sx15, red + lane * 68, (gi)); xsv = (lane >= PG * (gi) && lane < PG * (gi) + PG) ? xs : xsv; } while (0)
; __device__ __forceinline__ void peer3_dots(const u4 (&R)[PG][2], const u4 (&xq)[2], int sx15, LAS int* redrow, int g) {
;     static_assert(PG == 4, "one 16-byte LDS store per row group");
;     int d[4];
; #pragma unroll
;     for (int k = 0; k < 4; ++k) { int a = 0, ah = 0;
; #pragma unroll
;         for (int q = 0; q < 4; ++q) { const unsigned w = R[k][0][q];
;             a = __builtin_amdgcn_sdot4((int)(w & 0x0f0f0f0fu), (int)xq[0][q], a, false); ah = __builtin_amdgcn_sdot4((int)(w & 0xf0f0f0f0u), (int)xq[1][q], ah, false); }
;         d[k] = 32 * a + 2 * ah - sx15; }
;     u4 w; w.x = (unsigned)d[0]; w.y = (unsigned)d[1]; w.z = (unsigned)d[2]; w.w = (unsigned)d[3];
;     *(LAS u4*)(redrow + 4 * g) = w;
; }
; __device__ __forceinline__ void phase_peer_bucket(const Params& P, unsigned char* ws, int l, LAS unsigned char* lds, int bid, int G, int lane, int wave) {
;     ...
;             bool pre = false; u4 A[PG][2], B[PG][2], C[PG][2], Dq[PG][2];
; #pragma unroll 1
;             for (int blk = 0; blk < total; blk += 64) { const int blen = (total - blk) < 64 ? (total - blk) : 64, ng = blen / PG;
;                 const int ev = evn; const float wv = wvn;
;                 if (blk + 64 + lane < total) { evn = __builtin_nontemporal_load(FE + blk + 64 + lane); wvn = __builtin_nontemporal_load(FW + blk + 64 + lane); }
;                 const float us = USC[ev], vs = VSC[ev];
;                 float xsv = 0.f;
;                 if (ng == 16) {
;                     const bool nextfull = blk + 128 <= total;
;                     if (!pre) { PU_ROWS(A, 0); PU_ROWS(B, 1); PU_ROWS(C, 2); }
; #pragma unroll 1
;                     for (int g = 0; g < 12; g += 4) {
;                         PU_ROWS(Dq, g + 3); PU_DO(A, g); PU_ROWS(A, g + 4); PU_DO(B, g + 1); PU_ROWS(B, g + 5); PU_DO(C, g + 2); PU_ROWS(C, g + 6); PU_DO(Dq, g + 3);
;                     }
;                     PU_ROWS(Dq, 15); PU_DO(A, 12); if (nextfull) PU_ROWS_N(A, 0); PU_DO(B, 13); if (nextfull) PU_ROWS_N(B, 1); PU_DO(C, 14); if (nextfull) PU_ROWS_N(C, 2); PU_DO(Dq, 15);
.Lq_std5:
	s_waitcnt vmcnt(8)
	v_and_b32_e32 v96, 0xf0f0f0f, v16
	v_and_b32_e32 v100, 0xf0f0f0f0, v16
	v_and_b32_e32 v97, 0xf0f0f0f, v17
	v_and_b32_e32 v101, 0xf0f0f0f0, v17
	v_dot4_i32_i8 v104, v96, v64, 0
	v_dot4_i32_i8 v105, v100, v68, 0
	v_and_b32_e32 v98, 0xf0f0f0f, v18
	v_and_b32_e32 v102, 0xf0f0f0f0, v18
	v_dot4_i32_i8 v104, v97, v65, v104
	v_dot4_i32_i8 v105, v101, v69, v105
	v_and_b32_e32 v99, 0xf0f0f0f, v19
	v_and_b32_e32 v103, 0xf0f0f0f0, v19
	v_dot4_i32_i8 v104, v98, v66, v104
	v_dot4_i32_i8 v105, v102, v70, v105
	v_dot4_i32_i8 v104, v99, v67, v104
	v_dot4_i32_i8 v105, v103, v71, v105
	v_and_b32_e32 v96, 0xf0f0f0f, v20
	v_and_b32_e32 v100, 0xf0f0f0f0, v20
	v_and_b32_e32 v97, 0xf0f0f0f, v21
	v_and_b32_e32 v101, 0xf0f0f0f0, v21
	v_lshl_add_u32 v106, v104, 4, v105
	v_lshl_add_u32 v92, v106, 1, v72
	v_dot4_i32_i8 v126, v96, v64, 0
	v_dot4_i32_i8 v127, v100, v68, 0
	v_and_b32_e32 v98, 0xf0f0f0f, v22
	v_and_b32_e32 v102, 0xf0f0f0f0, v22
	v_dot4_i32_i8 v126, v97, v65, v126
	v_dot4_i32_i8 v127, v101, v69, v127
	v_and_b32_e32 v99, 0xf0f0f0f, v23
	v_and_b32_e32 v103, 0xf0f0f0f0, v23
	v_dot4_i32_i8 v126, v98, v66, v126
	v_dot4_i32_i8 v127, v102, v70, v127
	v_dot4_i32_i8 v126, v99, v67, v126
	v_dot4_i32_i8 v127, v103, v71, v127
	v_and_b32_e32 v96, 0xf0f0f0f, v24
	v_and_b32_e32 v100, 0xf0f0f0f0, v24
	v_and_b32_e32 v97, 0xf0f0f0f, v25
	v_and_b32_e32 v101, 0xf0f0f0f0, v25
	v_lshl_add_u32 v106, v126, 4, v127
	v_lshl_add_u32 v93, v106, 1, v72
	v_dot4_i32_i8 v104, v96, v64, 0
	v_dot4_i32_i8 v105, v100, v68, 0
	v_and_b32_e32 v98, 0xf0f0f0f, v26
	v_and_b32_e32 v102, 0xf0f0f0f0, v26
	v_dot4_i32_i8 v104, v97, v65, v104
	v_dot4_i32_i8 v105, v101, v69, v105
	v_and_b32_e32 v99, 0xf0f0f0f, v27
	v_and_b32_e32 v103, 0xf0f0f0f0, v27
	v_dot4_i32_i8 v104, v98, v66, v104
	v_dot4_i32_i8 v105, v102, v70, v105
	v_dot4_i32_i8 v104, v99, v67, v104
	v_dot4_i32_i8 v105, v103, v71, v105
	v_and_b32_e32 v96, 0xf0f0f0f, v28
	v_and_b32_e32 v100, 0xf0f0f0f0, v28
	v_and_b32_e32 v97, 0xf0f0f0f, v29
	v_and_b32_e32 v101, 0xf0f0f0f0, v29
	v_lshl_add_u32 v106, v104, 4, v105
	v_lshl_add_u32 v94, v106, 1, v72
	v_dot4_i32_i8 v126, v96, v64, 0
	v_dot4_i32_i8 v127, v100, v68, 0
	v_and_b32_e32 v98, 0xf0f0f0f, v30
	v_and_b32_e32 v102, 0xf0f0f0f0, v30
	v_dot4_i32_i8 v126, v97, v65, v126
	v_dot4_i32_i8 v127, v101, v69, v127
	v_and_b32_e32 v99, 0xf0f0f0f, v31
	v_and_b32_e32 v103, 0xf0f0f0f0, v31
	v_dot4_i32_i8 v126, v98, v66, v126
	v_dot4_i32_i8 v127, v102, v70, v127
	v_dot4_i32_i8 v126, v99, v67, v126
	v_dot4_i32_i8 v127, v103, v71, v127
	s_nop 0
	v_readlane_b32 s36, v75, 32
	v_readlane_b32 s5, v75, 33
	v_readlane_b32 s6, v75, 34
	v_readlane_b32 s7, v75, 35
	v_lshl_add_u32 v106, v126, 4, v127
	v_lshl_add_u32 v95, v106, 1, v72
	v_add_u32_e32 v113, s36, v206
	v_add_u32_e32 v114, s5, v206
	v_add_u32_e32 v115, s6, v206
	v_add_u32_e32 v116, s7, v206
	global_load_dwordx4 v[0:3], v113, s[52:53]
	global_load_dwordx4 v[4:7], v114, s[52:53]
	global_load_dwordx4 v[8:11], v115, s[52:53]
	global_load_dwordx4 v[12:15], v116, s[52:53]
	ds_write_b128 v107, v[92:95] offset:80
	s_lshl_b64 exec, s[22:23], 20
	v_mov_b32_e32 v87, s10
	s_mov_b64 exec, -1
.Lq_g6:
	s_add_u32 s11, s34, 24
	s_cmp_ge_u32 s11, s35
	s_cbranch_scc1 .Lq_sw6

; #define LAS __attribute__((address_space(3)))
; #define PU_DO(R, gi) do { PU_SWITCH(R, gi) peer3_dots(R, xq, sx15, red + lane * 68, (gi)); xsv = (lane >= PG * (gi) && lane < PG * (gi) + PG) ? xs : xsv; } while (0)
; __device__ __forceinline__ void peer3_dots(const u4 (&R)[PG][2], const u4 (&xq)[2], int sx15, LAS int* redrow, int g) {
;     static_assert(PG == 4, "one 16-byte LDS store per row group");
;     int d[4];
; #pragma unroll
;     for (int k = 0; k < 4; ++k) { int a = 0, ah = 0;
; #pragma unroll
;         for (int q = 0; q < 4; ++q) { const unsigned w = R[k][0][q];
;             a = __builtin_amdgcn_sdot4((int)(w & 0x0f0f0f0fu), (int)xq[0][q], a, false); ah = __builtin_amdgcn_sdot4((int)(w & 0xf0f0f0f0u), (int)xq[1][q], ah, false); }
;         d[k] = 32 * a + 2 * ah - sx15; }
;     u4 w; w.x = (unsigned)d[0]; w.y = (unsigned)d[1]; w.z = (unsigned)d[2]; w.w = (unsigned)d[3];
;     *(LAS u4*)(redrow + 4 * g) = w;
; }
; __device__ __forceinline__ void phase_peer_bucket(const Params& P, unsigned char* ws, int l, LAS unsigned char* lds, int bid, int G, int lane, int wave) {
;     ...
;             bool pre = false; u4 A[PG][2], B[PG][2], C[PG][2], Dq[PG][2];
; #pragma unroll 1
;             for (int blk = 0; blk < total; blk += 64) { const int blen = (total - blk) < 64 ? (total - blk) : 64, ng = blen / PG;
;                 const int ev = evn; const float wv = wvn;
;                 if (blk + 64 + lane < total) { evn = __builtin_nontemporal_load(FE + blk + 64 + lane); wvn = __builtin_nontemporal_load(FW + blk + 64 + lane); }
;                 const float us = USC[ev], vs = VSC[ev];
;                 float xsv = 0.f;
;                 if (ng == 16) {
;                     const bool nextfull = blk + 128 <= total;
;                     if (!pre) { PU_ROWS(A, 0); PU_ROWS(B, 1); PU_ROWS(C, 2); }
; #pragma unroll 1
;                     for (int g = 0; g < 12; g += 4) {
;                         PU_ROWS(Dq, g + 3); PU_DO(A, g); PU_ROWS(A, g + 4); PU_DO(B, g + 1); PU_ROWS(B, g + 5); PU_DO(C, g + 2); PU_ROWS(C, g + 6); PU_DO(Dq, g + 3);
;                     }
;                     PU_ROWS(Dq, 15); PU_DO(A, 12); if (nextfull) PU_ROWS_N(A, 0); PU_DO(B, 13); if (nextfull) PU_ROWS_N(B, 1); PU_DO(C, 14); if (nextfull) PU_ROWS_N(C, 2); PU_DO(Dq, 15);
.Lq_std6:
	s_waitcnt vmcnt(8)
	v_and_b32_e32 v96, 0xf0f0f0f, v32
	v_and_b32_e32 v100, 0xf0f0f0f0, v32
	v_and_b32_e32 v97, 0xf0f0f0f, v33
	v_and_b32_e32 v101, 0xf0f0f0f0, v33
	v_dot4_i32_i8 v104, v96, v64, 0
	v_dot4_i32_i8 v105, v100, v68, 0
	v_and_b32_e32 v98, 0xf0f0f0f, v34
	v_and_b32_e32 v102, 0xf0f0f0f0, v34
	v_dot4_i32_i8 v104, v97, v65, v104
	v_dot4_i32_i8 v105, v101, v69, v105
	v_and_b32_e32 v99, 0xf0f0f0f, v35
	v_and_b32_e32 v103, 0xf0f0f0f0, v35
	v_dot4_i32_i8 v104, v98, v66, v104
	v_dot4_i32_i8 v105, v102, v70, v105
	v_dot4_i32_i8 v104, v99, v67, v104
	v_dot4_i32_i8 v105, v103, v71, v105
	v_and_b32_e32 v96, 0xf0f0f0f, v36
	v_and_b32_e32 v100, 0xf0f0f0f0, v36
	v_and_b32_e32 v97, 0xf0f0f0f, v37
	v_and_b32_e32 v101, 0xf0f0f0f0, v37
	v_lshl_add_u32 v106, v104, 4, v105
	v_lshl_add_u32 v92, v106, 1, v72
	v_dot4_i32_i8 v126, v96, v64, 0
	v_dot4_i32_i8 v127, v100, v68, 0
	v_and_b32_e32 v98, 0xf0f0f0f, v38
	v_and_b32_e32 v102, 0xf0f0f0f0, v38
	v_dot4_i32_i8 v126, v97, v65, v126
	v_dot4_i32_i8 v127, v101, v69, v127
	v_and_b32_e32 v99, 0xf0f0f0f, v39
	v_and_b32_e32 v103, 0xf0f0f0f0, v39
	v_dot4_i32_i8 v126, v98, v66, v126
	v_dot4_i32_i8 v127, v102, v70, v127
	v_dot4_i32_i8 v126, v99, v67, v126
	v_dot4_i32_i8 v127, v103, v71, v127
	v_and_b32_e32 v96, 0xf0f0f0f, v40
	v_and_b32_e32 v100, 0xf0f0f0f0, v40
	v_and_b32_e32 v97, 0xf0f0f0f, v41
	v_and_b32_e32 v101, 0xf0f0f0f0, v41
	v_lshl_add_u32 v106, v126, 4, v127
	v_lshl_add_u32 v93, v106, 1, v72
	v_dot4_i32_i8 v104, v96, v64, 0
	v_dot4_i32_i8 v105, v100, v68, 0
	v_and_b32_e32 v98, 0xf0f0f0f, v42
	v_and_b32_e32 v102, 0xf0f0f0f0, v42
	v_dot4_i32_i8 v104, v97, v65, v104
	v_dot4_i32_i8 v105, v101, v69, v105
	v_and_b32_e32 v99, 0xf0f0f0f, v43
	v_and_b32_e32 v103, 0xf0f0f0f0, v43
	v_dot4_i32_i8 v104, v98, v66, v104
	v_dot4_i32_i8 v105, v102, v70, v105
	v_dot4_i32_i8 v104, v99, v67, v104
	v_dot4_i32_i8 v105, v103, v71, v105
	v_and_b32_e32 v96, 0xf0f0f0f, v44
	v_and_b32_e32 v100, 0xf0f0f0f0, v44
	v_and_b32_e32 v97, 0xf0f0f0f, v45
	v_and_b32_e32 v101, 0xf0f0f0f0, v45
	v_lshl_add_u32 v106, v104, 4, v105
	v_lshl_add_u32 v94, v106, 1, v72
	v_dot4_i32_i8 v126, v96, v64, 0
	v_dot4_i32_i8 v127, v100, v68, 0
	v_and_b32_e32 v98, 0xf0f0f0f, v46
	v_and_b32_e32 v102, 0xf0f0f0f0, v46
	v_dot4_i32_i8 v126, v97, v65, v126
	v_dot4_i32_i8 v127, v101, v69, v127
	v_and_b32_e32 v99, 0xf0f0f0f, v47
	v_and_b32_e32 v103, 0xf0f0f0f0, v47
	v_dot4_i32_i8 v126, v98, v66, v126
	v_dot4_i32_i8 v127, v102, v70, v127
	v_dot4_i32_i8 v126, v99, v67, v126
	v_dot4_i32_i8 v127, v103, v71, v127
	s_nop 0
	v_readlane_b32 s36, v75, 36
	v_readlane_b32 s5, v75, 37
	v_readlane_b32 s6, v75, 38
	v_readlane_b32 s7, v75, 39
	v_lshl_add_u32 v106, v126, 4, v127
	v_lshl_add_u32 v95, v106, 1, v72
	v_add_u32_e32 v113, s36, v206
	v_add_u32_e32 v114, s5, v206
	v_add_u32_e32 v115, s6, v206
	v_add_u32_e32 v116, s7, v206
	global_load_dwordx4 v[16:19], v113, s[52:53]
	global_load_dwordx4 v[20:23], v114, s[52:53]
	global_load_dwordx4 v[24:27], v115, s[52:53]
	global_load_dwordx4 v[28:31], v116, s[52:53]
	ds_write_b128 v107, v[92:95] offset:96
	s_lshl_b64 exec, s[22:23], 24
	v_mov_b32_e32 v87, s10
	s_mov_b64 exec, -1
.Lq_g7:
	s_add_u32 s11, s34, 28
	s_cmp_ge_u32 s11, s35
	s_cbranch_scc1 .Lq_sw7

; #define LAS __attribute__((address_space(3)))
; #define PU_DO(R, gi) do { PU_SWITCH(R, gi) peer3_dots(R, xq, sx15, red + lane * 68, (gi)); xsv = (lane >= PG * (gi) && lane < PG * (gi) + PG) ? xs : xsv; } while (0)
; __device__ __forceinline__ void peer3_dots(const u4 (&R)[PG][2], const u4 (&xq)[2], int sx15, LAS int* redrow, int g) {
;     static_assert(PG == 4, "one 16-byte LDS store per row group");
;     int d[4];
; #pragma unroll
;     for (int k = 0; k < 4; ++k) { int a = 0, ah = 0;
; #pragma unroll
;         for (int q = 0; q < 4; ++q) { const unsigned w = R[k][0][q];
;             a = __builtin_amdgcn_sdot4((int)(w & 0x0f0f0f0fu), (int)xq[0][q], a, false); ah = __builtin_amdgcn_sdot4((int)(w & 0xf0f0f0f0u), (int)xq[1][q], ah, false); }
;         d[k] = 32 * a + 2 * ah - sx15; }
;     u4 w; w.x = (unsigned)d[0]; w.y = (unsigned)d[1]; w.z = (unsigned)d[2]; w.w = (unsigned)d[3];
;     *(LAS u4*)(redrow + 4 * g) = w;
; }
; __device__ __forceinline__ void phase_peer_bucket(const Params& P, unsigned char* ws, int l, LAS unsigned char* lds, int bid, int G, int lane, int wave) {
;     ...
;             bool pre = false; u4 A[PG][2], B[PG][2], C[PG][2], Dq[PG][2];
; #pragma unroll 1
;             for (int blk = 0; blk < total; blk += 64) { const int blen = (total - blk) < 64 ? (total - blk) : 64, ng = blen / PG;
;                 const int ev = evn; const float wv = wvn;
;                 if (blk + 64 + lane < total) { evn = __builtin_nontemporal_load(FE + blk + 64 + lane); wvn = __builtin_nontemporal_load(FW + blk + 64 + lane); }
;                 const float us = USC[ev], vs = VSC[ev];
;                 float xsv = 0.f;
;                 if (ng == 16) {
;                     const bool nextfull = blk + 128 <= total;
;                     if (!pre) { PU_ROWS(A, 0); PU_ROWS(B, 1); PU_ROWS(C, 2); }
; #pragma unroll 1
;                     for (int g = 0; g < 12; g += 4) {
;                         PU_ROWS(Dq, g + 3); PU_DO(A, g); PU_ROWS(A, g + 4); PU_DO(B, g + 1); PU_ROWS(B, g + 5); PU_DO(C, g + 2); PU_ROWS(C, g + 6); PU_DO(Dq, g + 3);
;                     }
;                     PU_ROWS(Dq, 15); PU_DO(A, 12); if (nextfull) PU_ROWS_N(A, 0); PU_DO(B, 13); if (nextfull) PU_ROWS_N(B, 1); PU_DO(C, 14); if (nextfull) PU_ROWS_N(C, 2); PU_DO(Dq, 15);
.Lq_std7:
	s_waitcnt vmcnt(8)
	v_and_b32_e32 v96, 0xf0f0f0f, v48
	v_and_b32_e32 v100, 0xf0f0f0f0, v48
	v_and_b32_e32 v97, 0xf0f0f0f, v49
	v_and_b32_e32 v101, 0xf0f0f0f0, v49
	v_dot4_i32_i8 v104, v96, v64, 0
	v_dot4_i32_i8 v105, v100, v68, 0
	v_and_b32_e32 v98, 0xf0f0f0f, v50
	v_and_b32_e32 v102, 0xf0f0f0f0, v50
	v_dot4_i32_i8 v104, v97, v65, v104
	v_dot4_i32_i8 v105, v101, v69, v105
	v_and_b32_e32 v99, 0xf0f0f0f, v51
	v_and_b32_e32 v103, 0xf0f0f0f0, v51
	v_dot4_i32_i8 v104, v98, v66, v104
	v_dot4_i32_i8 v105, v102, v70, v105
	v_dot4_i32_i8 v104, v99, v67, v104
	v_dot4_i32_i8 v105, v103, v71, v105
	v_and_b32_e32 v96, 0xf0f0f0f, v52
	v_and_b32_e32 v100, 0xf0f0f0f0, v52
	v_and_b32_e32 v97, 0xf0f0f0f, v53
	v_and_b32_e32 v101, 0xf0f0f0f0, v53
	v_lshl_add_u32 v106, v104, 4, v105
	v_lshl_add_u32 v92, v106, 1, v72
	v_dot4_i32_i8 v126, v96, v64, 0
	v_dot4_i32_i8 v127, v100, v68, 0
	v_and_b32_e32 v98, 0xf0f0f0f, v54
	v_and_b32_e32 v102, 0xf0f0f0f0, v54
	v_dot4_i32_i8 v126, v97, v65, v126
	v_dot4_i32_i8 v127, v101, v69, v127
	v_and_b32_e32 v99, 0xf0f0f0f, v55
	v_and_b32_e32 v103, 0xf0f0f0f0, v55
	v_dot4_i32_i8 v126, v98, v66, v126
	v_dot4_i32_i8 v127, v102, v70, v127
	v_dot4_i32_i8 v126, v99, v67, v126
	v_dot4_i32_i8 v127, v103, v71, v127
	v_and_b32_e32 v96, 0xf0f0f0f, v56
	v_and_b32_e32 v100, 0xf0f0f0f0, v56
	v_and_b32_e32 v97, 0xf0f0f0f, v57
	v_and_b32_e32 v101, 0xf0f0f0f0, v57
	v_lshl_add_u32 v106, v126, 4, v127
	v_lshl_add_u32 v93, v106, 1, v72
	v_dot4_i32_i8 v104, v96, v64, 0
	v_dot4_i32_i8 v105, v100, v68, 0
	v_and_b32_e32 v98, 0xf0f0f0f, v58
	v_and_b32_e32 v102, 0xf0f0f0f0, v58
	v_dot4_i32_i8 v104, v97, v65, v104
	v_dot4_i32_i8 v105, v101, v69, v105
	v_and_b32_e32 v99, 0xf0f0f0f, v59
	v_and_b32_e32 v103, 0xf0f0f0f0, v59
	v_dot4_i32_i8 v104, v98, v66, v104
	v_dot4_i32_i8 v105, v102, v70, v105
	v_dot4_i32_i8 v104, v99, v67, v104
	v_dot4_i32_i8 v105, v103, v71, v105
	v_and_b32_e32 v96, 0xf0f0f0f, v60
	v_and_b32_e32 v100, 0xf0f0f0f0, v60
	v_and_b32_e32 v97, 0xf0f0f0f, v61
	v_and_b32_e32 v101, 0xf0f0f0f0, v61
	v_lshl_add_u32 v106, v104, 4, v105
	v_lshl_add_u32 v94, v106, 1, v72
	v_dot4_i32_i8 v126, v96, v64, 0
	v_dot4_i32_i8 v127, v100, v68, 0
	v_and_b32_e32 v98, 0xf0f0f0f, v62
	v_and_b32_e32 v102, 0xf0f0f0f0, v62
	v_dot4_i32_i8 v126, v97, v65, v126
	v_dot4_i32_i8 v127, v101, v69, v127
	v_and_b32_e32 v99, 0xf0f0f0f, v63
	v_and_b32_e32 v103, 0xf0f0f0f0, v63
	v_dot4_i32_i8 v126, v98, v66, v126
	v_dot4_i32_i8 v127, v102, v70, v127
	v_dot4_i32_i8 v126, v99, v67, v126
	v_dot4_i32_i8 v127, v103, v71, v127
	s_nop 0
	v_readlane_b32 s36, v75, 40
	v_readlane_b32 s5, v75, 41
	v_readlane_b32 s6, v75, 42
	v_readlane_b32 s7, v75, 43
	v_lshl_add_u32 v106, v126, 4, v127
	v_lshl_add_u32 v95, v106, 1, v72
	v_add_u32_e32 v113, s36, v206
	v_add_u32_e32 v114, s5, v206
	v_add_u32_e32 v115, s6, v206
	v_add_u32_e32 v116, s7, v206
	global_load_dwordx4 v[32:35], v113, s[52:53]
	global_load_dwordx4 v[36:39], v114, s[52:53]
	global_load_dwordx4 v[40:43], v115, s[52:53]
	global_load_dwordx4 v[44:47], v116, s[52:53]
	ds_write_b128 v107, v[92:95] offset:112
	s_lshl_b64 exec, s[22:23], 28
	v_mov_b32_e32 v87, s10
	s_mov_b64 exec, -1
.Lq_g8:
	s_add_u32 s11, s34, 32
	s_cmp_ge_u32 s11, s35
	s_cbranch_scc1 .Lq_sw8

; #define LAS __attribute__((address_space(3)))
; #define PU_DO(R, gi) do { PU_SWITCH(R, gi) peer3_dots(R, xq, sx15, red + lane * 68, (gi)); xsv = (lane >= PG * (gi) && lane < PG * (gi) + PG) ? xs : xsv; } while (0)
; __device__ __forceinline__ void peer3_dots(const u4 (&R)[PG][2], const u4 (&xq)[2], int sx15, LAS int* redrow, int g) {
;     static_assert(PG == 4, "one 16-byte LDS store per row group");
;     int d[4];
; #pragma unroll
;     for (int k = 0; k < 4; ++k) { int a = 0, ah = 0;
; #pragma unroll
;         for (int q = 0; q < 4; ++q) { const unsigned w = R[k][0][q];
;             a = __builtin_amdgcn_sdot4((int)(w & 0x0f0f0f0fu), (int)xq[0][q], a, false); ah = __builtin_amdgcn_sdot4((int)(w & 0xf0f0f0f0u), (int)xq[1][q], ah, false); }
;         d[k] = 32 * a + 2 * ah - sx15; }
;     u4 w; w.x = (unsigned)d[0]; w.y = (unsigned)d[1]; w.z = (unsigned)d[2]; w.w = (unsigned)d[3];
;     *(LAS u4*)(redrow + 4 * g) = w;
; }
; __device__ __forceinline__ void phase_peer_bucket(const Params& P, unsigned char* ws, int l, LAS unsigned char* lds, int bid, int G, int lane, int wave) {
;     ...
;             bool pre = false; u4 A[PG][2], B[PG][2], C[PG][2], Dq[PG][2];
; #pragma unroll 1
;             for (int blk = 0; blk < total; blk += 64) { const int blen = (total - blk) < 64 ? (total - blk) : 64, ng = blen / PG;
;                 const int ev = evn; const float wv = wvn;
;                 if (blk + 64 + lane < total) { evn = __builtin_nontemporal_load(FE + blk + 64 + lane); wvn = __builtin_nontemporal_load(FW + blk + 64 + lane); }
;                 const float us = USC[ev], vs = VSC[ev];
;                 float xsv = 0.f;
;                 if (ng == 16) {
;                     const bool nextfull = blk + 128 <= total;
;                     if (!pre) { PU_ROWS(A, 0); PU_ROWS(B, 1); PU_ROWS(C, 2); }
; #pragma unroll 1
;                     for (int g = 0; g < 12; g += 4) {
;                         PU_ROWS(Dq, g + 3); PU_DO(A, g); PU_ROWS(A, g + 4); PU_DO(B, g + 1); PU_ROWS(B, g + 5); PU_DO(C, g + 2); PU_ROWS(C, g + 6); PU_DO(Dq, g + 3);
;                     }
;                     PU_ROWS(Dq, 15); PU_DO(A, 12); if (nextfull) PU_ROWS_N(A, 0); PU_DO(B, 13); if (nextfull) PU_ROWS_N(B, 1); PU_DO(C, 14); if (nextfull) PU_ROWS_N(C, 2); PU_DO(Dq, 15);
.Lq_std8:
	s_waitcnt vmcnt(8)
	v_and_b32_e32 v96, 0xf0f0f0f, v0
	v_and_b32_e32 v100, 0xf0f0f0f0, v0
	v_and_b32_e32 v97, 0xf0f0f0f, v1
	v_and_b32_e32 v101, 0xf0f0f0f0, v1
	v_dot4_i32_i8 v104, v96, v64, 0
	v_dot4_i32_i8 v105, v100, v68, 0
	v_and_b32_e32 v98, 0xf0f0f0f, v2
	v_and_b32_e32 v102, 0xf0f0f0f0, v2
	v_dot4_i32_i8 v104, v97, v65, v104
	v_dot4_i32_i8 v105, v101, v69, v105
	v_and_b32_e32 v99, 0xf0f0f0f, v3
	v_and_b32_e32 v103, 0xf0f0f0f0, v3
	v_dot4_i32_i8 v104, v98, v66, v104
	v_dot4_i32_i8 v105, v102, v70, v105
	v_dot4_i32_i8 v104, v99, v67, v104
	v_dot4_i32_i8 v105, v103, v71, v105
	v_and_b32_e32 v96, 0xf0f0f0f, v4
	v_and_b32_e32 v100, 0xf0f0f0f0, v4
	v_and_b32_e32 v97, 0xf0f0f0f, v5
	v_and_b32_e32 v101, 0xf0f0f0f0, v5
	v_lshl_add_u32 v106, v104, 4, v105
	v_lshl_add_u32 v92, v106, 1, v72
	v_dot4_i32_i8 v126, v96, v64, 0
	v_dot4_i32_i8 v127, v100, v68, 0
	v_and_b32_e32 v98, 0xf0f0f0f, v6
	v_and_b32_e32 v102, 0xf0f0f0f0, v6
	v_dot4_i32_i8 v126, v97, v65, v126
	v_dot4_i32_i8 v127, v101, v69, v127
	v_and_b32_e32 v99, 0xf0f0f0f, v7
	v_and_b32_e32 v103, 0xf0f0f0f0, v7
	v_dot4_i32_i8 v126, v98, v66, v126
	v_dot4_i32_i8 v127, v102, v70, v127
	v_dot4_i32_i8 v126, v99, v67, v126
	v_dot4_i32_i8 v127, v103, v71, v127
	v_and_b32_e32 v96, 0xf0f0f0f, v8
	v_and_b32_e32 v100, 0xf0f0f0f0, v8
	v_and_b32_e32 v97, 0xf0f0f0f, v9
	v_and_b32_e32 v101, 0xf0f0f0f0, v9
	v_lshl_add_u32 v106, v126, 4, v127
	v_lshl_add_u32 v93, v106, 1, v72
	v_dot4_i32_i8 v104, v96, v64, 0
	v_dot4_i32_i8 v105, v100, v68, 0
	v_and_b32_e32 v98, 0xf0f0f0f, v10
	v_and_b32_e32 v102, 0xf0f0f0f0, v10
	v_dot4_i32_i8 v104, v97, v65, v104
	v_dot4_i32_i8 v105, v101, v69, v105
	v_and_b32_e32 v99, 0xf0f0f0f, v11
	v_and_b32_e32 v103, 0xf0f0f0f0, v11
	v_dot4_i32_i8 v104, v98, v66, v104
	v_dot4_i32_i8 v105, v102, v70, v105
	v_dot4_i32_i8 v104, v99, v67, v104
	v_dot4_i32_i8 v105, v103, v71, v105
	v_and_b32_e32 v96, 0xf0f0f0f, v12
	v_and_b32_e32 v100, 0xf0f0f0f0, v12
	v_and_b32_e32 v97, 0xf0f0f0f, v13
	v_and_b32_e32 v101, 0xf0f0f0f0, v13
	v_lshl_add_u32 v106, v104, 4, v105
	v_lshl_add_u32 v94, v106, 1, v72
	v_dot4_i32_i8 v126, v96, v64, 0
	v_dot4_i32_i8 v127, v100, v68, 0
	v_and_b32_e32 v98, 0xf0f0f0f, v14
	v_and_b32_e32 v102, 0xf0f0f0f0, v14
	v_dot4_i32_i8 v126, v97, v65, v126
	v_dot4_i32_i8 v127, v101, v69, v127
	v_and_b32_e32 v99, 0xf0f0f0f, v15
	v_and_b32_e32 v103, 0xf0f0f0f0, v15
	v_dot4_i32_i8 v126, v98, v66, v126
	v_dot4_i32_i8 v127, v102, v70, v127
	v_dot4_i32_i8 v126, v99, v67, v126
	v_dot4_i32_i8 v127, v103, v71, v127
	s_nop 0
	v_readlane_b32 s36, v75, 44
	v_readlane_b32 s5, v75, 45
	v_readlane_b32 s6, v75, 46
	v_readlane_b32 s7, v75, 47
	v_lshl_add_u32 v106, v126, 4, v127
	v_lshl_add_u32 v95, v106, 1, v72
	v_add_u32_e32 v113, s36, v206
	v_add_u32_e32 v114, s5, v206
	v_add_u32_e32 v115, s6, v206
	v_add_u32_e32 v116, s7, v206
	global_load_dwordx4 v[48:51], v113, s[52:53]
	global_load_dwordx4 v[52:55], v114, s[52:53]
	global_load_dwordx4 v[56:59], v115, s[52:53]
	global_load_dwordx4 v[60:63], v116, s[52:53]
	ds_write_b128 v107, v[92:95] offset:128
	s_lshl_b64 exec, s[22:23], 32
	v_mov_b32_e32 v87, s10
	s_mov_b64 exec, -1
.Lq_g9:
	s_add_u32 s11, s34, 36
	s_cmp_ge_u32 s11, s35
	s_cbranch_scc1 .Lq_sw9

; #define LAS __attribute__((address_space(3)))
; #define PU_DO(R, gi) do { PU_SWITCH(R, gi) peer3_dots(R, xq, sx15, red + lane * 68, (gi)); xsv = (lane >= PG * (gi) && lane < PG * (gi) + PG) ? xs : xsv; } while (0)
; __device__ __forceinline__ void peer3_dots(const u4 (&R)[PG][2], const u4 (&xq)[2], int sx15, LAS int* redrow, int g) {
;     static_assert(PG == 4, "one 16-byte LDS store per row group");
;     int d[4];
; #pragma unroll
;     for (int k = 0; k < 4; ++k) { int a = 0, ah = 0;
; #pragma unroll
;         for (int q = 0; q < 4; ++q) { const unsigned w = R[k][0][q];
;             a = __builtin_amdgcn_sdot4((int)(w & 0x0f0f0f0fu), (int)xq[0][q], a, false); ah = __builtin_amdgcn_sdot4((int)(w & 0xf0f0f0f0u), (int)xq[1][q], ah, false); }
;         d[k] = 32 * a + 2 * ah - sx15; }
;     u4 w; w.x = (unsigned)d[0]; w.y = (unsigned)d[1]; w.z = (unsigned)d[2]; w.w = (unsigned)d[3];
;     *(LAS u4*)(redrow + 4 * g) = w;
; }
; __device__ __forceinline__ void phase_peer_bucket(const Params& P, unsigned char* ws, int l, LAS unsigned char* lds, int bid, int G, int lane, int wave) {
;     ...
;             bool pre = false; u4 A[PG][2], B[PG][2], C[PG][2], Dq[PG][2];
; #pragma unroll 1
;             for (int blk = 0; blk < total; blk += 64) { const int blen = (total - blk) < 64 ? (total - blk) : 64, ng = blen / PG;
;                 const int ev = evn; const float wv = wvn;
;                 if (blk + 64 + lane < total) { evn = __builtin_nontemporal_load(FE + blk + 64 + lane); wvn = __builtin_nontemporal_load(FW + blk + 64 + lane); }
;                 const float us = USC[ev], vs = VSC[ev];
;                 float xsv = 0.f;
;                 if (ng == 16) {
;                     const bool nextfull = blk + 128 <= total;
;                     if (!pre) { PU_ROWS(A, 0); PU_ROWS(B, 1); PU_ROWS(C, 2); }
; #pragma unroll 1
;                     for (int g = 0; g < 12; g += 4) {
;                         PU_ROWS(Dq, g + 3); PU_DO(A, g); PU_ROWS(A, g + 4); PU_DO(B, g + 1); PU_ROWS(B, g + 5); PU_DO(C, g + 2); PU_ROWS(C, g + 6); PU_DO(Dq, g + 3);
;                     }
;                     PU_ROWS(Dq, 15); PU_DO(A, 12); if (nextfull) PU_ROWS_N(A, 0); PU_DO(B, 13); if (nextfull) PU_ROWS_N(B, 1); PU_DO(C, 14); if (nextfull) PU_ROWS_N(C, 2); PU_DO(Dq, 15);
.Lq_std9:
	s_waitcnt vmcnt(8)
	v_and_b32_e32 v96, 0xf0f0f0f, v16
	v_and_b32_e32 v100, 0xf0f0f0f0, v16
	v_and_b32_e32 v97, 0xf0f0f0f, v17
	v_and_b32_e32 v101, 0xf0f0f0f0, v17
	v_dot4_i32_i8 v104, v96, v64, 0
	v_dot4_i32_i8 v105, v100, v68, 0
	v_and_b32_e32 v98, 0xf0f0f0f, v18
	v_and_b32_e32 v102, 0xf0f0f0f0, v18
	v_dot4_i32_i8 v104, v97, v65, v104
	v_dot4_i32_i8 v105, v101, v69, v105
	v_and_b32_e32 v99, 0xf0f0f0f, v19
	v_and_b32_e32 v103, 0xf0f0f0f0, v19
	v_dot4_i32_i8 v104, v98, v66, v104
	v_dot4_i32_i8 v105, v102, v70, v105
	v_dot4_i32_i8 v104, v99, v67, v104
	v_dot4_i32_i8 v105, v103, v71, v105
	v_and_b32_e32 v96, 0xf0f0f0f, v20
	v_and_b32_e32 v100, 0xf0f0f0f0, v20
	v_and_b32_e32 v97, 0xf0f0f0f, v21
	v_and_b32_e32 v101, 0xf0f0f0f0, v21
	v_lshl_add_u32 v106, v104, 4, v105
	v_lshl_add_u32 v92, v106, 1, v72
	v_dot4_i32_i8 v126, v96, v64, 0
	v_dot4_i32_i8 v127, v100, v68, 0
	v_and_b32_e32 v98, 0xf0f0f0f, v22
	v_and_b32_e32 v102, 0xf0f0f0f0, v22
	v_dot4_i32_i8 v126, v97, v65, v126
	v_dot4_i32_i8 v127, v101, v69, v127
	v_and_b32_e32 v99, 0xf0f0f0f, v23
	v_and_b32_e32 v103, 0xf0f0f0f0, v23
	v_dot4_i32_i8 v126, v98, v66, v126
	v_dot4_i32_i8 v127, v102, v70, v127
	v_dot4_i32_i8 v126, v99, v67, v126
	v_dot4_i32_i8 v127, v103, v71, v127
	v_and_b32_e32 v96, 0xf0f0f0f, v24
	v_and_b32_e32 v100, 0xf0f0f0f0, v24
	v_and_b32_e32 v97, 0xf0f0f0f, v25
	v_and_b32_e32 v101, 0xf0f0f0f0, v25
	v_lshl_add_u32 v106, v126, 4, v127
	v_lshl_add_u32 v93, v106, 1, v72
	v_dot4_i32_i8 v104, v96, v64, 0
	v_dot4_i32_i8 v105, v100, v68, 0
	v_and_b32_e32 v98, 0xf0f0f0f, v26
	v_and_b32_e32 v102, 0xf0f0f0f0, v26
	v_dot4_i32_i8 v104, v97, v65, v104
	v_dot4_i32_i8 v105, v101, v69, v105
	v_and_b32_e32 v99, 0xf0f0f0f, v27
	v_and_b32_e32 v103, 0xf0f0f0f0, v27
	v_dot4_i32_i8 v104, v98, v66, v104
	v_dot4_i32_i8 v105, v102, v70, v105
	v_dot4_i32_i8 v104, v99, v67, v104
	v_dot4_i32_i8 v105, v103, v71, v105
	v_and_b32_e32 v96, 0xf0f0f0f, v28
	v_and_b32_e32 v100, 0xf0f0f0f0, v28
	v_and_b32_e32 v97, 0xf0f0f0f, v29
	v_and_b32_e32 v101, 0xf0f0f0f0, v29
	v_lshl_add_u32 v106, v104, 4, v105
	v_lshl_add_u32 v94, v106, 1, v72
	v_dot4_i32_i8 v126, v96, v64, 0
	v_dot4_i32_i8 v127, v100, v68, 0
	v_and_b32_e32 v98, 0xf0f0f0f, v30
	v_and_b32_e32 v102, 0xf0f0f0f0, v30
	v_dot4_i32_i8 v126, v97, v65, v126
	v_dot4_i32_i8 v127, v101, v69, v127
	v_and_b32_e32 v99, 0xf0f0f0f, v31
	v_and_b32_e32 v103, 0xf0f0f0f0, v31
	v_dot4_i32_i8 v126, v98, v66, v126
	v_dot4_i32_i8 v127, v102, v70, v127
	v_dot4_i32_i8 v126, v99, v67, v126
	v_dot4_i32_i8 v127, v103, v71, v127
	s_nop 0
	v_readlane_b32 s36, v75, 48
	v_readlane_b32 s5, v75, 49
	v_readlane_b32 s6, v75, 50
	v_readlane_b32 s7, v75, 51
	v_lshl_add_u32 v106, v126, 4, v127
	v_lshl_add_u32 v95, v106, 1, v72
	v_add_u32_e32 v113, s36, v206
	v_add_u32_e32 v114, s5, v206
	v_add_u32_e32 v115, s6, v206
	v_add_u32_e32 v116, s7, v206
	global_load_dwordx4 v[0:3], v113, s[52:53]
	global_load_dwordx4 v[4:7], v114, s[52:53]
	global_load_dwordx4 v[8:11], v115, s[52:53]
	global_load_dwordx4 v[12:15], v116, s[52:53]
	ds_write_b128 v107, v[92:95] offset:144
	s_lshl_b64 exec, s[22:23], 36
	v_mov_b32_e32 v87, s10
	s_mov_b64 exec, -1
.Lq_g10:
	s_add_u32 s11, s34, 40
	s_cmp_ge_u32 s11, s35
	s_cbranch_scc1 .Lq_sw10

; #define LAS __attribute__((address_space(3)))
; #define PU_DO(R, gi) do { PU_SWITCH(R, gi) peer3_dots(R, xq, sx15, red + lane * 68, (gi)); xsv = (lane >= PG * (gi) && lane < PG * (gi) + PG) ? xs : xsv; } while (0)
; __device__ __forceinline__ void peer3_dots(const u4 (&R)[PG][2], const u4 (&xq)[2], int sx15, LAS int* redrow, int g) {
;     static_assert(PG == 4, "one 16-byte LDS store per row group");
;     int d[4];
; #pragma unroll
;     for (int k = 0; k < 4; ++k) { int a = 0, ah = 0;
; #pragma unroll
;         for (int q = 0; q < 4; ++q) { const unsigned w = R[k][0][q];
;             a = __builtin_amdgcn_sdot4((int)(w & 0x0f0f0f0fu), (int)xq[0][q], a, false); ah = __builtin_amdgcn_sdot4((int)(w & 0xf0f0f0f0u), (int)xq[1][q], ah, false); }
;         d[k] = 32 * a + 2 * ah - sx15; }
;     u4 w; w.x = (unsigned)d[0]; w.y = (unsigned)d[1]; w.z = (unsigned)d[2]; w.w = (unsigned)d[3];
;     *(LAS u4*)(redrow + 4 * g) = w;
; }
; __device__ __forceinline__ void phase_peer_bucket(const Params& P, unsigned char* ws, int l, LAS unsigned char* lds, int bid, int G, int lane, int wave) {
;     ...
;             bool pre = false; u4 A[PG][2], B[PG][2], C[PG][2], Dq[PG][2];
; #pragma unroll 1
;             for (int blk = 0; blk < total; blk += 64) { const int blen = (total - blk) < 64 ? (total - blk) : 64, ng = blen / PG;
;                 const int ev = evn; const float wv = wvn;
;                 if (blk + 64 + lane < total) { evn = __builtin_nontemporal_load(FE + blk + 64 + lane); wvn = __builtin_nontemporal_load(FW + blk + 64 + lane); }
;                 const float us = USC[ev], vs = VSC[ev];
;                 float xsv = 0.f;
;                 if (ng == 16) {
;                     const bool nextfull = blk + 128 <= total;
;                     if (!pre) { PU_ROWS(A, 0); PU_ROWS(B, 1); PU_ROWS(C, 2); }
; #pragma unroll 1
;                     for (int g = 0; g < 12; g += 4) {
;                         PU_ROWS(Dq, g + 3); PU_DO(A, g); PU_ROWS(A, g + 4); PU_DO(B, g + 1); PU_ROWS(B, g + 5); PU_DO(C, g + 2); PU_ROWS(C, g + 6); PU_DO(Dq, g + 3);
;                     }
;                     PU_ROWS(Dq, 15); PU_DO(A, 12); if (nextfull) PU_ROWS_N(A, 0); PU_DO(B, 13); if (nextfull) PU_ROWS_N(B, 1); PU_DO(C, 14); if (nextfull) PU_ROWS_N(C, 2); PU_DO(Dq, 15);
.Lq_std10:
	s_waitcnt vmcnt(8)
	v_and_b32_e32 v96, 0xf0f0f0f, v32
	v_and_b32_e32 v100, 0xf0f0f0f0, v32
	v_and_b32_e32 v97, 0xf0f0f0f, v33
	v_and_b32_e32 v101, 0xf0f0f0f0, v33
	v_dot4_i32_i8 v104, v96, v64, 0
	v_dot4_i32_i8 v105, v100, v68, 0
	v_and_b32_e32 v98, 0xf0f0f0f, v34
	v_and_b32_e32 v102, 0xf0f0f0f0, v34
	v_dot4_i32_i8 v104, v97, v65, v104
	v_dot4_i32_i8 v105, v101, v69, v105
	v_and_b32_e32 v99, 0xf0f0f0f, v35
	v_and_b32_e32 v103, 0xf0f0f0f0, v35
	v_dot4_i32_i8 v104, v98, v66, v104
	v_dot4_i32_i8 v105, v102, v70, v105
	v_dot4_i32_i8 v104, v99, v67, v104
	v_dot4_i32_i8 v105, v103, v71, v105
	v_and_b32_e32 v96, 0xf0f0f0f, v36
	v_and_b32_e32 v100, 0xf0f0f0f0, v36
	v_and_b32_e32 v97, 0xf0f0f0f, v37
	v_and_b32_e32 v101, 0xf0f0f0f0, v37
	v_lshl_add_u32 v106, v104, 4, v105
	v_lshl_add_u32 v92, v106, 1, v72
	v_dot4_i32_i8 v126, v96, v64, 0
	v_dot4_i32_i8 v127, v100, v68, 0
	v_and_b32_e32 v98, 0xf0f0f0f, v38
	v_and_b32_e32 v102, 0xf0f0f0f0, v38
	v_dot4_i32_i8 v126, v97, v65, v126
	v_dot4_i32_i8 v127, v101, v69, v127
	v_and_b32_e32 v99, 0xf0f0f0f, v39
	v_and_b32_e32 v103, 0xf0f0f0f0, v39
	v_dot4_i32_i8 v126, v98, v66, v126
	v_dot4_i32_i8 v127, v102, v70, v127
	v_dot4_i32_i8 v126, v99, v67, v126
	v_dot4_i32_i8 v127, v103, v71, v127
	v_and_b32_e32 v96, 0xf0f0f0f, v40
	v_and_b32_e32 v100, 0xf0f0f0f0, v40
	v_and_b32_e32 v97, 0xf0f0f0f, v41
	v_and_b32_e32 v101, 0xf0f0f0f0, v41
	v_lshl_add_u32 v106, v126, 4, v127
	v_lshl_add_u32 v93, v106, 1, v72
	v_dot4_i32_i8 v104, v96, v64, 0
	v_dot4_i32_i8 v105, v100, v68, 0
	v_and_b32_e32 v98, 0xf0f0f0f, v42
	v_and_b32_e32 v102, 0xf0f0f0f0, v42
	v_dot4_i32_i8 v104, v97, v65, v104
	v_dot4_i32_i8 v105, v101, v69, v105
	v_and_b32_e32 v99, 0xf0f0f0f, v43
	v_and_b32_e32 v103, 0xf0f0f0f0, v43
	v_dot4_i32_i8 v104, v98, v66, v104
	v_dot4_i32_i8 v105, v102, v70, v105
	v_dot4_i32_i8 v104, v99, v67, v104
	v_dot4_i32_i8 v105, v103, v71, v105
	v_and_b32_e32 v96, 0xf0f0f0f, v44
	v_and_b32_e32 v100, 0xf0f0f0f0, v44
	v_and_b32_e32 v97, 0xf0f0f0f, v45
	v_and_b32_e32 v101, 0xf0f0f0f0, v45
	v_lshl_add_u32 v106, v104, 4, v105
	v_lshl_add_u32 v94, v106, 1, v72
	v_dot4_i32_i8 v126, v96, v64, 0
	v_dot4_i32_i8 v127, v100, v68, 0
	v_and_b32_e32 v98, 0xf0f0f0f, v46
	v_and_b32_e32 v102, 0xf0f0f0f0, v46
	v_dot4_i32_i8 v126, v97, v65, v126
	v_dot4_i32_i8 v127, v101, v69, v127
	v_and_b32_e32 v99, 0xf0f0f0f, v47
	v_and_b32_e32 v103, 0xf0f0f0f0, v47
	v_dot4_i32_i8 v126, v98, v66, v126
	v_dot4_i32_i8 v127, v102, v70, v127
	v_dot4_i32_i8 v126, v99, v67, v126
	v_dot4_i32_i8 v127, v103, v71, v127
	s_nop 0
	v_readlane_b32 s36, v75, 52
	v_readlane_b32 s5, v75, 53
	v_readlane_b32 s6, v75, 54
	v_readlane_b32 s7, v75, 55
	v_lshl_add_u32 v106, v126, 4, v127
	v_lshl_add_u32 v95, v106, 1, v72
	v_add_u32_e32 v113, s36, v206
	v_add_u32_e32 v114, s5, v206
	v_add_u32_e32 v115, s6, v206
	v_add_u32_e32 v116, s7, v206
	global_load_dwordx4 v[16:19], v113, s[52:53]
	global_load_dwordx4 v[20:23], v114, s[52:53]
	global_load_dwordx4 v[24:27], v115, s[52:53]
	global_load_dwordx4 v[28:31], v116, s[52:53]
	ds_write_b128 v107, v[92:95] offset:160
	s_lshl_b64 exec, s[22:23], 40
	v_mov_b32_e32 v87, s10
	s_mov_b64 exec, -1
.Lq_g11:
	s_add_u32 s11, s34, 44
	s_cmp_ge_u32 s11, s35
	s_cbranch_scc1 .Lq_sw11

; #define LAS __attribute__((address_space(3)))
; #define PU_DO(R, gi) do { PU_SWITCH(R, gi) peer3_dots(R, xq, sx15, red + lane * 68, (gi)); xsv = (lane >= PG * (gi) && lane < PG * (gi) + PG) ? xs : xsv; } while (0)
; __device__ __forceinline__ void peer3_dots(const u4 (&R)[PG][2], const u4 (&xq)[2], int sx15, LAS int* redrow, int g) {
;     static_assert(PG == 4, "one 16-byte LDS store per row group");
;     int d[4];
; #pragma unroll
;     for (int k = 0; k < 4; ++k) { int a = 0, ah = 0;
; #pragma unroll
;         for (int q = 0; q < 4; ++q) { const unsigned w = R[k][0][q];
;             a = __builtin_amdgcn_sdot4((int)(w & 0x0f0f0f0fu), (int)xq[0][q], a, false); ah = __builtin_amdgcn_sdot4((int)(w & 0xf0f0f0f0u), (int)xq[1][q], ah, false); }
;         d[k] = 32 * a + 2 * ah - sx15; }
;     u4 w; w.x = (unsigned)d[0]; w.y = (unsigned)d[1]; w.z = (unsigned)d[2]; w.w = (unsigned)d[3];
;     *(LAS u4*)(redrow + 4 * g) = w;
; }
; __device__ __forceinline__ void phase_peer_bucket(const Params& P, unsigned char* ws, int l, LAS unsigned char* lds, int bid, int G, int lane, int wave) {
;     ...
;             bool pre = false; u4 A[PG][2], B[PG][2], C[PG][2], Dq[PG][2];
; #pragma unroll 1
;             for (int blk = 0; blk < total; blk += 64) { const int blen = (total - blk) < 64 ? (total - blk) : 64, ng = blen / PG;
;                 const int ev = evn; const float wv = wvn;
;                 if (blk + 64 + lane < total) { evn = __builtin_nontemporal_load(FE + blk + 64 + lane); wvn = __builtin_nontemporal_load(FW + blk + 64 + lane); }
;                 const float us = USC[ev], vs = VSC[ev];
;                 float xsv = 0.f;
;                 if (ng == 16) {
;                     const bool nextfull = blk + 128 <= total;
;                     if (!pre) { PU_ROWS(A, 0); PU_ROWS(B, 1); PU_ROWS(C, 2); }
; #pragma unroll 1
;                     for (int g = 0; g < 12; g += 4) {
;                         PU_ROWS(Dq, g + 3); PU_DO(A, g); PU_ROWS(A, g + 4); PU_DO(B, g + 1); PU_ROWS(B, g + 5); PU_DO(C, g + 2); PU_ROWS(C, g + 6); PU_DO(Dq, g + 3);
;                     }
;                     PU_ROWS(Dq, 15); PU_DO(A, 12); if (nextfull) PU_ROWS_N(A, 0); PU_DO(B, 13); if (nextfull) PU_ROWS_N(B, 1); PU_DO(C, 14); if (nextfull) PU_ROWS_N(C, 2); PU_DO(Dq, 15);
.Lq_std11:
	s_waitcnt vmcnt(8)
	v_and_b32_e32 v96, 0xf0f0f0f, v48
	v_and_b32_e32 v100, 0xf0f0f0f0, v48
	v_and_b32_e32 v97, 0xf0f0f0f, v49
	v_and_b32_e32 v101, 0xf0f0f0f0, v49
	v_dot4_i32_i8 v104, v96, v64, 0
	v_dot4_i32_i8 v105, v100, v68, 0
	v_and_b32_e32 v98, 0xf0f0f0f, v50
	v_and_b32_e32 v102, 0xf0f0f0f0, v50
	v_dot4_i32_i8 v104, v97, v65, v104
	v_dot4_i32_i8 v105, v101, v69, v105
	v_and_b32_e32 v99, 0xf0f0f0f, v51
	v_and_b32_e32 v103, 0xf0f0f0f0, v51
	v_dot4_i32_i8 v104, v98, v66, v104
	v_dot4_i32_i8 v105, v102, v70, v105
	v_dot4_i32_i8 v104, v99, v67, v104
	v_dot4_i32_i8 v105, v103, v71, v105
	v_and_b32_e32 v96, 0xf0f0f0f, v52
	v_and_b32_e32 v100, 0xf0f0f0f0, v52
	v_and_b32_e32 v97, 0xf0f0f0f, v53
	v_and_b32_e32 v101, 0xf0f0f0f0, v53
	v_lshl_add_u32 v106, v104, 4, v105
	v_lshl_add_u32 v92, v106, 1, v72
	v_dot4_i32_i8 v126, v96, v64, 0
	v_dot4_i32_i8 v127, v100, v68, 0
	v_and_b32_e32 v98, 0xf0f0f0f, v54
	v_and_b32_e32 v102, 0xf0f0f0f0, v54
	v_dot4_i32_i8 v126, v97, v65, v126
	v_dot4_i32_i8 v127, v101, v69, v127
	v_and_b32_e32 v99, 0xf0f0f0f, v55
	v_and_b32_e32 v103, 0xf0f0f0f0, v55
	v_dot4_i32_i8 v126, v98, v66, v126
	v_dot4_i32_i8 v127, v102, v70, v127
	v_dot4_i32_i8 v126, v99, v67, v126
	v_dot4_i32_i8 v127, v103, v71, v127
	v_and_b32_e32 v96, 0xf0f0f0f, v56
	v_and_b32_e32 v100, 0xf0f0f0f0, v56
	v_and_b32_e32 v97, 0xf0f0f0f, v57
	v_and_b32_e32 v101, 0xf0f0f0f0, v57
	v_lshl_add_u32 v106, v126, 4, v127
	v_lshl_add_u32 v93, v106, 1, v72
	v_dot4_i32_i8 v104, v96, v64, 0
	v_dot4_i32_i8 v105, v100, v68, 0
	v_and_b32_e32 v98, 0xf0f0f0f, v58
	v_and_b32_e32 v102, 0xf0f0f0f0, v58
	v_dot4_i32_i8 v104, v97, v65, v104
	v_dot4_i32_i8 v105, v101, v69, v105
	v_and_b32_e32 v99, 0xf0f0f0f, v59
	v_and_b32_e32 v103, 0xf0f0f0f0, v59
	v_dot4_i32_i8 v104, v98, v66, v104
	v_dot4_i32_i8 v105, v102, v70, v105
	v_dot4_i32_i8 v104, v99, v67, v104
	v_dot4_i32_i8 v105, v103, v71, v105
	v_and_b32_e32 v96, 0xf0f0f0f, v60
	v_and_b32_e32 v100, 0xf0f0f0f0, v60
	v_and_b32_e32 v97, 0xf0f0f0f, v61
	v_and_b32_e32 v101, 0xf0f0f0f0, v61
	v_lshl_add_u32 v106, v104, 4, v105
	v_lshl_add_u32 v94, v106, 1, v72
	v_dot4_i32_i8 v126, v96, v64, 0
	v_dot4_i32_i8 v127, v100, v68, 0
	v_and_b32_e32 v98, 0xf0f0f0f, v62
	v_and_b32_e32 v102, 0xf0f0f0f0, v62
	v_dot4_i32_i8 v126, v97, v65, v126
	v_dot4_i32_i8 v127, v101, v69, v127
	v_and_b32_e32 v99, 0xf0f0f0f, v63
	v_and_b32_e32 v103, 0xf0f0f0f0, v63
	v_dot4_i32_i8 v126, v98, v66, v126
	v_dot4_i32_i8 v127, v102, v70, v127
	v_dot4_i32_i8 v126, v99, v67, v126
	v_dot4_i32_i8 v127, v103, v71, v127
	s_nop 0
	v_readlane_b32 s36, v75, 56
	v_readlane_b32 s5, v75, 57
	v_readlane_b32 s6, v75, 58
	v_readlane_b32 s7, v75, 59
	v_lshl_add_u32 v106, v126, 4, v127
	v_lshl_add_u32 v95, v106, 1, v72
	v_add_u32_e32 v113, s36, v206
	v_add_u32_e32 v114, s5, v206
	v_add_u32_e32 v115, s6, v206
	v_add_u32_e32 v116, s7, v206
	global_load_dwordx4 v[32:35], v113, s[52:53]
	global_load_dwordx4 v[36:39], v114, s[52:53]
	global_load_dwordx4 v[40:43], v115, s[52:53]
	global_load_dwordx4 v[44:47], v116, s[52:53]
	ds_write_b128 v107, v[92:95] offset:176
	s_lshl_b64 exec, s[22:23], 44
	v_mov_b32_e32 v87, s10
	s_mov_b64 exec, -1
.Lq_g12:
	s_add_u32 s11, s34, 48
	s_cmp_ge_u32 s11, s35
	s_cbranch_scc1 .Lq_sw12

; #define LAS __attribute__((address_space(3)))
; #define PU_DO(R, gi) do { PU_SWITCH(R, gi) peer3_dots(R, xq, sx15, red + lane * 68, (gi)); xsv = (lane >= PG * (gi) && lane < PG * (gi) + PG) ? xs : xsv; } while (0)
; __device__ __forceinline__ void peer3_dots(const u4 (&R)[PG][2], const u4 (&xq)[2], int sx15, LAS int* redrow, int g) {
;     static_assert(PG == 4, "one 16-byte LDS store per row group");
;     int d[4];
; #pragma unroll
;     for (int k = 0; k < 4; ++k) { int a = 0, ah = 0;
; #pragma unroll
;         for (int q = 0; q < 4; ++q) { const unsigned w = R[k][0][q];
;             a = __builtin_amdgcn_sdot4((int)(w & 0x0f0f0f0fu), (int)xq[0][q], a, false); ah = __builtin_amdgcn_sdot4((int)(w & 0xf0f0f0f0u), (int)xq[1][q], ah, false); }
;         d[k] = 32 * a + 2 * ah - sx15; }
;     u4 w; w.x = (unsigned)d[0]; w.y = (unsigned)d[1]; w.z = (unsigned)d[2]; w.w = (unsigned)d[3];
;     *(LAS u4*)(redrow + 4 * g) = w;
; }
; __device__ __forceinline__ void phase_peer_bucket(const Params& P, unsigned char* ws, int l, LAS unsigned char* lds, int bid, int G, int lane, int wave) {
;     ...
;             bool pre = false; u4 A[PG][2], B[PG][2], C[PG][2], Dq[PG][2];
; #pragma unroll 1
;             for (int blk = 0; blk < total; blk += 64) { const int blen = (total - blk) < 64 ? (total - blk) : 64, ng = blen / PG;
;                 const int ev = evn; const float wv = wvn;
;                 if (blk + 64 + lane < total) { evn = __builtin_nontemporal_load(FE + blk + 64 + lane); wvn = __builtin_nontemporal_load(FW + blk + 64 + lane); }
;                 const float us = USC[ev], vs = VSC[ev];
;                 float xsv = 0.f;
;                 if (ng == 16) {
;                     const bool nextfull = blk + 128 <= total;
;                     if (!pre) { PU_ROWS(A, 0); PU_ROWS(B, 1); PU_ROWS(C, 2); }
; #pragma unroll 1
;                     for (int g = 0; g < 12; g += 4) {
;                         PU_ROWS(Dq, g + 3); PU_DO(A, g); PU_ROWS(A, g + 4); PU_DO(B, g + 1); PU_ROWS(B, g + 5); PU_DO(C, g + 2); PU_ROWS(C, g + 6); PU_DO(Dq, g + 3);
;                     }
;                     PU_ROWS(Dq, 15); PU_DO(A, 12); if (nextfull) PU_ROWS_N(A, 0); PU_DO(B, 13); if (nextfull) PU_ROWS_N(B, 1); PU_DO(C, 14); if (nextfull) PU_ROWS_N(C, 2); PU_DO(Dq, 15);
.Lq_std12:
	s_waitcnt vmcnt(8)
	v_and_b32_e32 v96, 0xf0f0f0f, v0
	v_and_b32_e32 v100, 0xf0f0f0f0, v0
	v_and_b32_e32 v97, 0xf0f0f0f, v1
	v_and_b32_e32 v101, 0xf0f0f0f0, v1
	v_dot4_i32_i8 v104, v96, v64, 0
	v_dot4_i32_i8 v105, v100, v68, 0
	v_and_b32_e32 v98, 0xf0f0f0f, v2
	v_and_b32_e32 v102, 0xf0f0f0f0, v2
	v_dot4_i32_i8 v104, v97, v65, v104
	v_dot4_i32_i8 v105, v101, v69, v105
	v_and_b32_e32 v99, 0xf0f0f0f, v3
	v_and_b32_e32 v103, 0xf0f0f0f0, v3
	v_dot4_i32_i8 v104, v98, v66, v104
	v_dot4_i32_i8 v105, v102, v70, v105
	v_dot4_i32_i8 v104, v99, v67, v104
	v_dot4_i32_i8 v105, v103, v71, v105
	v_and_b32_e32 v96, 0xf0f0f0f, v4
	v_and_b32_e32 v100, 0xf0f0f0f0, v4
	v_and_b32_e32 v97, 0xf0f0f0f, v5
	v_and_b32_e32 v101, 0xf0f0f0f0, v5
	v_lshl_add_u32 v106, v104, 4, v105
	v_lshl_add_u32 v92, v106, 1, v72
	v_dot4_i32_i8 v126, v96, v64, 0
	v_dot4_i32_i8 v127, v100, v68, 0
	v_and_b32_e32 v98, 0xf0f0f0f, v6
	v_and_b32_e32 v102, 0xf0f0f0f0, v6
	v_dot4_i32_i8 v126, v97, v65, v126
	v_dot4_i32_i8 v127, v101, v69, v127
	v_and_b32_e32 v99, 0xf0f0f0f, v7
	v_and_b32_e32 v103, 0xf0f0f0f0, v7
	v_dot4_i32_i8 v126, v98, v66, v126
	v_dot4_i32_i8 v127, v102, v70, v127
	v_dot4_i32_i8 v126, v99, v67, v126
	v_dot4_i32_i8 v127, v103, v71, v127
	v_and_b32_e32 v96, 0xf0f0f0f, v8
	v_and_b32_e32 v100, 0xf0f0f0f0, v8
	v_and_b32_e32 v97, 0xf0f0f0f, v9
	v_and_b32_e32 v101, 0xf0f0f0f0, v9
	v_lshl_add_u32 v106, v126, 4, v127
	v_lshl_add_u32 v93, v106, 1, v72
	v_dot4_i32_i8 v104, v96, v64, 0
	v_dot4_i32_i8 v105, v100, v68, 0
	v_and_b32_e32 v98, 0xf0f0f0f, v10
	v_and_b32_e32 v102, 0xf0f0f0f0, v10
	v_dot4_i32_i8 v104, v97, v65, v104
	v_dot4_i32_i8 v105, v101, v69, v105
	v_and_b32_e32 v99, 0xf0f0f0f, v11
	v_and_b32_e32 v103, 0xf0f0f0f0, v11
	v_dot4_i32_i8 v104, v98, v66, v104
	v_dot4_i32_i8 v105, v102, v70, v105
	v_dot4_i32_i8 v104, v99, v67, v104
	v_dot4_i32_i8 v105, v103, v71, v105
	v_and_b32_e32 v96, 0xf0f0f0f, v12
	v_and_b32_e32 v100, 0xf0f0f0f0, v12
	v_and_b32_e32 v97, 0xf0f0f0f, v13
	v_and_b32_e32 v101, 0xf0f0f0f0, v13
	v_lshl_add_u32 v106, v104, 4, v105
	v_lshl_add_u32 v94, v106, 1, v72
	v_dot4_i32_i8 v126, v96, v64, 0
	v_dot4_i32_i8 v127, v100, v68, 0
	v_and_b32_e32 v98, 0xf0f0f0f, v14
	v_and_b32_e32 v102, 0xf0f0f0f0, v14
	v_dot4_i32_i8 v126, v97, v65, v126
	v_dot4_i32_i8 v127, v101, v69, v127
	v_and_b32_e32 v99, 0xf0f0f0f, v15
	v_and_b32_e32 v103, 0xf0f0f0f0, v15
	v_dot4_i32_i8 v126, v98, v66, v126
	v_dot4_i32_i8 v127, v102, v70, v127
	v_dot4_i32_i8 v126, v99, v67, v126
	v_dot4_i32_i8 v127, v103, v71, v127
	s_nop 0
	v_readlane_b32 s36, v75, 60
	v_readlane_b32 s5, v75, 61
	v_readlane_b32 s6, v75, 62
	v_readlane_b32 s7, v75, 63
	v_lshl_add_u32 v106, v126, 4, v127
	v_lshl_add_u32 v95, v106, 1, v72
	v_add_u32_e32 v113, s36, v206
	v_add_u32_e32 v114, s5, v206
	v_add_u32_e32 v115, s6, v206
	v_add_u32_e32 v116, s7, v206
	global_load_dwordx4 v[48:51], v113, s[52:53]
	global_load_dwordx4 v[52:55], v114, s[52:53]
	global_load_dwordx4 v[56:59], v115, s[52:53]
	global_load_dwordx4 v[60:63], v116, s[52:53]
	ds_write_b128 v107, v[92:95] offset:192
	s_lshl_b64 exec, s[22:23], 48
	v_mov_b32_e32 v87, s10
	s_mov_b64 exec, -1
.Lq_g13:
	s_add_u32 s11, s34, 52
	s_cmp_ge_u32 s11, s35
	s_cbranch_scc1 .Lq_sw13

; #define LAS __attribute__((address_space(3)))
; #define PU_DO(R, gi) do { PU_SWITCH(R, gi) peer3_dots(R, xq, sx15, red + lane * 68, (gi)); xsv = (lane >= PG * (gi) && lane < PG * (gi) + PG) ? xs : xsv; } while (0)
; __device__ __forceinline__ void peer3_dots(const u4 (&R)[PG][2], const u4 (&xq)[2], int sx15, LAS int* redrow, int g) {
;     static_assert(PG == 4, "one 16-byte LDS store per row group");
;     int d[4];
; #pragma unroll
;     for (int k = 0; k < 4; ++k) { int a = 0, ah = 0;
; #pragma unroll
;         for (int q = 0; q < 4; ++q) { const unsigned w = R[k][0][q];
;             a = __builtin_amdgcn_sdot4((int)(w & 0x0f0f0f0fu), (int)xq[0][q], a, false); ah = __builtin_amdgcn_sdot4((int)(w & 0xf0f0f0f0u), (int)xq[1][q], ah, false); }
;         d[k] = 32 * a + 2 * ah - sx15; }
;     u4 w; w.x = (unsigned)d[0]; w.y = (unsigned)d[1]; w.z = (unsigned)d[2]; w.w = (unsigned)d[3];
;     *(LAS u4*)(redrow + 4 * g) = w;
; }
; __device__ __forceinline__ void phase_peer_bucket(const Params& P, unsigned char* ws, int l, LAS unsigned char* lds, int bid, int G, int lane, int wave) {
;     ...
;             bool pre = false; u4 A[PG][2], B[PG][2], C[PG][2], Dq[PG][2];
; #pragma unroll 1
;             for (int blk = 0; blk < total; blk += 64) { const int blen = (total - blk) < 64 ? (total - blk) : 64, ng = blen / PG;
;                 const int ev = evn; const float wv = wvn;
;                 if (blk + 64 + lane < total) { evn = __builtin_nontemporal_load(FE + blk + 64 + lane); wvn = __builtin_nontemporal_load(FW + blk + 64 + lane); }
;                 const float us = USC[ev], vs = VSC[ev];
;                 float xsv = 0.f;
;                 if (ng == 16) {
;                     const bool nextfull = blk + 128 <= total;
;                     if (!pre) { PU_ROWS(A, 0); PU_ROWS(B, 1); PU_ROWS(C, 2); }
; #pragma unroll 1
;                     for (int g = 0; g < 12; g += 4) {
;                         PU_ROWS(Dq, g + 3); PU_DO(A, g); PU_ROWS(A, g + 4); PU_DO(B, g + 1); PU_ROWS(B, g + 5); PU_DO(C, g + 2); PU_ROWS(C, g + 6); PU_DO(Dq, g + 3);
;                     }
;                     PU_ROWS(Dq, 15); PU_DO(A, 12); if (nextfull) PU_ROWS_N(A, 0); PU_DO(B, 13); if (nextfull) PU_ROWS_N(B, 1); PU_DO(C, 14); if (nextfull) PU_ROWS_N(C, 2); PU_DO(Dq, 15);
.Lq_std13:
	s_waitcnt vmcnt(8)
	v_and_b32_e32 v96, 0xf0f0f0f, v16
	v_and_b32_e32 v100, 0xf0f0f0f0, v16
	v_and_b32_e32 v97, 0xf0f0f0f, v17
	v_and_b32_e32 v101, 0xf0f0f0f0, v17
	v_dot4_i32_i8 v104, v96, v64, 0
	v_dot4_i32_i8 v105, v100, v68, 0
	v_and_b32_e32 v98, 0xf0f0f0f, v18
	v_and_b32_e32 v102, 0xf0f0f0f0, v18
	v_dot4_i32_i8 v104, v97, v65, v104
	v_dot4_i32_i8 v105, v101, v69, v105
	v_and_b32_e32 v99, 0xf0f0f0f, v19
	v_and_b32_e32 v103, 0xf0f0f0f0, v19
	v_dot4_i32_i8 v104, v98, v66, v104
	v_dot4_i32_i8 v105, v102, v70, v105
	v_dot4_i32_i8 v104, v99, v67, v104
	v_dot4_i32_i8 v105, v103, v71, v105
	v_and_b32_e32 v96, 0xf0f0f0f, v20
	v_and_b32_e32 v100, 0xf0f0f0f0, v20
	v_and_b32_e32 v97, 0xf0f0f0f, v21
	v_and_b32_e32 v101, 0xf0f0f0f0, v21
	v_lshl_add_u32 v106, v104, 4, v105
	v_lshl_add_u32 v92, v106, 1, v72
	v_dot4_i32_i8 v126, v96, v64, 0
	v_dot4_i32_i8 v127, v100, v68, 0
	v_and_b32_e32 v98, 0xf0f0f0f, v22
	v_and_b32_e32 v102, 0xf0f0f0f0, v22
	v_dot4_i32_i8 v126, v97, v65, v126
	v_dot4_i32_i8 v127, v101, v69, v127
	v_and_b32_e32 v99, 0xf0f0f0f, v23
	v_and_b32_e32 v103, 0xf0f0f0f0, v23
	v_dot4_i32_i8 v126, v98, v66, v126
	v_dot4_i32_i8 v127, v102, v70, v127
	v_dot4_i32_i8 v126, v99, v67, v126
	v_dot4_i32_i8 v127, v103, v71, v127
	v_and_b32_e32 v96, 0xf0f0f0f, v24
	v_and_b32_e32 v100, 0xf0f0f0f0, v24
	v_and_b32_e32 v97, 0xf0f0f0f, v25
	v_and_b32_e32 v101, 0xf0f0f0f0, v25
	v_lshl_add_u32 v106, v126, 4, v127
	v_lshl_add_u32 v93, v106, 1, v72
	v_dot4_i32_i8 v104, v96, v64, 0
	v_dot4_i32_i8 v105, v100, v68, 0
	v_and_b32_e32 v98, 0xf0f0f0f, v26
	v_and_b32_e32 v102, 0xf0f0f0f0, v26
	v_dot4_i32_i8 v104, v97, v65, v104
	v_dot4_i32_i8 v105, v101, v69, v105
	v_and_b32_e32 v99, 0xf0f0f0f, v27
	v_and_b32_e32 v103, 0xf0f0f0f0, v27
	v_dot4_i32_i8 v104, v98, v66, v104
	v_dot4_i32_i8 v105, v102, v70, v105
	v_dot4_i32_i8 v104, v99, v67, v104
	v_dot4_i32_i8 v105, v103, v71, v105
	v_and_b32_e32 v96, 0xf0f0f0f, v28
	v_and_b32_e32 v100, 0xf0f0f0f0, v28
	v_and_b32_e32 v97, 0xf0f0f0f, v29
	v_and_b32_e32 v101, 0xf0f0f0f0, v29
	v_lshl_add_u32 v106, v104, 4, v105
	v_lshl_add_u32 v94, v106, 1, v72
	v_dot4_i32_i8 v126, v96, v64, 0
	v_dot4_i32_i8 v127, v100, v68, 0
	v_and_b32_e32 v98, 0xf0f0f0f, v30
	v_and_b32_e32 v102, 0xf0f0f0f0, v30
	v_dot4_i32_i8 v126, v97, v65, v126
	v_dot4_i32_i8 v127, v101, v69, v127
	v_and_b32_e32 v99, 0xf0f0f0f, v31
	v_and_b32_e32 v103, 0xf0f0f0f0, v31
	v_dot4_i32_i8 v126, v98, v66, v126
	v_dot4_i32_i8 v127, v102, v70, v127
	v_dot4_i32_i8 v126, v99, v67, v126
	v_dot4_i32_i8 v127, v103, v71, v127
	v_lshlrev_b32_e32 v76, 10, v74
	s_nop 0
	v_readlane_b32 s36, v76, 0
	v_readlane_b32 s5, v76, 1
	v_readlane_b32 s6, v76, 2
	v_readlane_b32 s7, v76, 3
	v_lshl_add_u32 v106, v126, 4, v127
	v_lshl_add_u32 v95, v106, 1, v72
	v_add_u32_e32 v113, s36, v206
	v_add_u32_e32 v114, s5, v206
	v_add_u32_e32 v115, s6, v206
	v_add_u32_e32 v116, s7, v206
	global_load_dwordx4 v[0:3], v113, s[52:53]
	global_load_dwordx4 v[4:7], v114, s[52:53]
	global_load_dwordx4 v[8:11], v115, s[52:53]
	global_load_dwordx4 v[12:15], v116, s[52:53]
	ds_write_b128 v107, v[92:95] offset:208
	s_lshl_b64 exec, s[22:23], 52
	v_mov_b32_e32 v87, s10
	s_mov_b64 exec, -1
.Lq_g14:
	s_add_u32 s11, s34, 56
	s_cmp_ge_u32 s11, s35
	s_cbranch_scc1 .Lq_sw14

; #define LAS __attribute__((address_space(3)))
; #define PU_DO(R, gi) do { PU_SWITCH(R, gi) peer3_dots(R, xq, sx15, red + lane * 68, (gi)); xsv = (lane >= PG * (gi) && lane < PG * (gi) + PG) ? xs : xsv; } while (0)
; __device__ __forceinline__ void peer3_dots(const u4 (&R)[PG][2], const u4 (&xq)[2], int sx15, LAS int* redrow, int g) {
;     static_assert(PG == 4, "one 16-byte LDS store per row group");
;     int d[4];
; #pragma unroll
;     for (int k = 0; k < 4; ++k) { int a = 0, ah = 0;
; #pragma unroll
;         for (int q = 0; q < 4; ++q) { const unsigned w = R[k][0][q];
;             a = __builtin_amdgcn_sdot4((int)(w & 0x0f0f0f0fu), (int)xq[0][q], a, false); ah = __builtin_amdgcn_sdot4((int)(w & 0xf0f0f0f0u), (int)xq[1][q], ah, false); }
;         d[k] = 32 * a + 2 * ah - sx15; }
;     u4 w; w.x = (unsigned)d[0]; w.y = (unsigned)d[1]; w.z = (unsigned)d[2]; w.w = (unsigned)d[3];
;     *(LAS u4*)(redrow + 4 * g) = w;
; }
; __device__ __forceinline__ void phase_peer_bucket(const Params& P, unsigned char* ws, int l, LAS unsigned char* lds, int bid, int G, int lane, int wave) {
;     ...
;             bool pre = false; u4 A[PG][2], B[PG][2], C[PG][2], Dq[PG][2];
; #pragma unroll 1
;             for (int blk = 0; blk < total; blk += 64) { const int blen = (total - blk) < 64 ? (total - blk) : 64, ng = blen / PG;
;                 const int ev = evn; const float wv = wvn;
;                 if (blk + 64 + lane < total) { evn = __builtin_nontemporal_load(FE + blk + 64 + lane); wvn = __builtin_nontemporal_load(FW + blk + 64 + lane); }
;                 const float us = USC[ev], vs = VSC[ev];
;                 float xsv = 0.f;
;                 if (ng == 16) {
;                     const bool nextfull = blk + 128 <= total;
;                     if (!pre) { PU_ROWS(A, 0); PU_ROWS(B, 1); PU_ROWS(C, 2); }
; #pragma unroll 1
;                     for (int g = 0; g < 12; g += 4) {
;                         PU_ROWS(Dq, g + 3); PU_DO(A, g); PU_ROWS(A, g + 4); PU_DO(B, g + 1); PU_ROWS(B, g + 5); PU_DO(C, g + 2); PU_ROWS(C, g + 6); PU_DO(Dq, g + 3);
;                     }
;                     PU_ROWS(Dq, 15); PU_DO(A, 12); if (nextfull) PU_ROWS_N(A, 0); PU_DO(B, 13); if (nextfull) PU_ROWS_N(B, 1); PU_DO(C, 14); if (nextfull) PU_ROWS_N(C, 2); PU_DO(Dq, 15);
.Lq_std14:
	s_waitcnt vmcnt(8)
	v_and_b32_e32 v96, 0xf0f0f0f, v32
	v_and_b32_e32 v100, 0xf0f0f0f0, v32
	v_and_b32_e32 v97, 0xf0f0f0f, v33
	v_and_b32_e32 v101, 0xf0f0f0f0, v33
	v_dot4_i32_i8 v104, v96, v64, 0
	v_dot4_i32_i8 v105, v100, v68, 0
	v_and_b32_e32 v98, 0xf0f0f0f, v34
	v_and_b32_e32 v102, 0xf0f0f0f0, v34
	v_dot4_i32_i8 v104, v97, v65, v104
	v_dot4_i32_i8 v105, v101, v69, v105
	v_and_b32_e32 v99, 0xf0f0f0f, v35
	v_and_b32_e32 v103, 0xf0f0f0f0, v35
	v_dot4_i32_i8 v104, v98, v66, v104
	v_dot4_i32_i8 v105, v102, v70, v105
	v_dot4_i32_i8 v104, v99, v67, v104
	v_dot4_i32_i8 v105, v103, v71, v105
	v_and_b32_e32 v96, 0xf0f0f0f, v36
	v_and_b32_e32 v100, 0xf0f0f0f0, v36
	v_and_b32_e32 v97, 0xf0f0f0f, v37
	v_and_b32_e32 v101, 0xf0f0f0f0, v37
	v_lshl_add_u32 v106, v104, 4, v105
	v_lshl_add_u32 v92, v106, 1, v72
	v_dot4_i32_i8 v126, v96, v64, 0
	v_dot4_i32_i8 v127, v100, v68, 0
	v_and_b32_e32 v98, 0xf0f0f0f, v38
	v_and_b32_e32 v102, 0xf0f0f0f0, v38
	v_dot4_i32_i8 v126, v97, v65, v126
	v_dot4_i32_i8 v127, v101, v69, v127
	v_and_b32_e32 v99, 0xf0f0f0f, v39
	v_and_b32_e32 v103, 0xf0f0f0f0, v39
	v_dot4_i32_i8 v126, v98, v66, v126
	v_dot4_i32_i8 v127, v102, v70, v127
	v_dot4_i32_i8 v126, v99, v67, v126
	v_dot4_i32_i8 v127, v103, v71, v127
	v_and_b32_e32 v96, 0xf0f0f0f, v40
	v_and_b32_e32 v100, 0xf0f0f0f0, v40
	v_and_b32_e32 v97, 0xf0f0f0f, v41
	v_and_b32_e32 v101, 0xf0f0f0f0, v41
	v_lshl_add_u32 v106, v126, 4, v127
	v_lshl_add_u32 v93, v106, 1, v72
	v_dot4_i32_i8 v104, v96, v64, 0
	v_dot4_i32_i8 v105, v100, v68, 0
	v_and_b32_e32 v98, 0xf0f0f0f, v42
	v_and_b32_e32 v102, 0xf0f0f0f0, v42
	v_dot4_i32_i8 v104, v97, v65, v104
	v_dot4_i32_i8 v105, v101, v69, v105
	v_and_b32_e32 v99, 0xf0f0f0f, v43
	v_and_b32_e32 v103, 0xf0f0f0f0, v43
	v_dot4_i32_i8 v104, v98, v66, v104
	v_dot4_i32_i8 v105, v102, v70, v105
	v_dot4_i32_i8 v104, v99, v67, v104
	v_dot4_i32_i8 v105, v103, v71, v105
	v_and_b32_e32 v96, 0xf0f0f0f, v44
	v_and_b32_e32 v100, 0xf0f0f0f0, v44
	v_and_b32_e32 v97, 0xf0f0f0f, v45
	v_and_b32_e32 v101, 0xf0f0f0f0, v45
	v_lshl_add_u32 v106, v104, 4, v105
	v_lshl_add_u32 v94, v106, 1, v72
	v_dot4_i32_i8 v126, v96, v64, 0
	v_dot4_i32_i8 v127, v100, v68, 0
	v_and_b32_e32 v98, 0xf0f0f0f, v46
	v_and_b32_e32 v102, 0xf0f0f0f0, v46
	v_dot4_i32_i8 v126, v97, v65, v126
	v_dot4_i32_i8 v127, v101, v69, v127
	v_and_b32_e32 v99, 0xf0f0f0f, v47
	v_and_b32_e32 v103, 0xf0f0f0f0, v47
	v_dot4_i32_i8 v126, v98, v66, v126
	v_dot4_i32_i8 v127, v102, v70, v127
	v_dot4_i32_i8 v126, v99, v67, v126
	v_dot4_i32_i8 v127, v103, v71, v127
	s_nop 0
	v_readlane_b32 s36, v76, 4
	v_readlane_b32 s5, v76, 5
	v_readlane_b32 s6, v76, 6
	v_readlane_b32 s7, v76, 7
	v_lshl_add_u32 v106, v126, 4, v127
	v_lshl_add_u32 v95, v106, 1, v72
	v_add_u32_e32 v113, s36, v206
	v_add_u32_e32 v114, s5, v206
	v_add_u32_e32 v115, s6, v206
	v_add_u32_e32 v116, s7, v206
	global_load_dwordx4 v[16:19], v113, s[52:53]
	global_load_dwordx4 v[20:23], v114, s[52:53]
	global_load_dwordx4 v[24:27], v115, s[52:53]
	global_load_dwordx4 v[28:31], v116, s[52:53]
	ds_write_b128 v107, v[92:95] offset:224
	s_lshl_b64 exec, s[22:23], 56
	v_mov_b32_e32 v87, s10
	s_mov_b64 exec, -1
.Lq_g15:
	s_add_u32 s11, s34, 60
	s_cmp_ge_u32 s11, s35
	s_cbranch_scc1 .Lq_sw15

; #define LAS __attribute__((address_space(3)))
; #define PU_DO(R, gi) do { PU_SWITCH(R, gi) peer3_dots(R, xq, sx15, red + lane * 68, (gi)); xsv = (lane >= PG * (gi) && lane < PG * (gi) + PG) ? xs : xsv; } while (0)
; __device__ __forceinline__ void peer3_dots(const u4 (&R)[PG][2], const u4 (&xq)[2], int sx15, LAS int* redrow, int g) {
;     static_assert(PG == 4, "one 16-byte LDS store per row group");
;     int d[4];
; #pragma unroll
;     for (int k = 0; k < 4; ++k) { int a = 0, ah = 0;
; #pragma unroll
;         for (int q = 0; q < 4; ++q) { const unsigned w = R[k][0][q];
;             a = __builtin_amdgcn_sdot4((int)(w & 0x0f0f0f0fu), (int)xq[0][q], a, false); ah = __builtin_amdgcn_sdot4((int)(w & 0xf0f0f0f0u), (int)xq[1][q], ah, false); }
;         d[k] = 32 * a + 2 * ah - sx15; }
;     u4 w; w.x = (unsigned)d[0]; w.y = (unsigned)d[1]; w.z = (unsigned)d[2]; w.w = (unsigned)d[3];
;     *(LAS u4*)(redrow + 4 * g) = w;
; }
; __device__ __forceinline__ void phase_peer_bucket(const Params& P, unsigned char* ws, int l, LAS unsigned char* lds, int bid, int G, int lane, int wave) {
;     ...
;             bool pre = false; u4 A[PG][2], B[PG][2], C[PG][2], Dq[PG][2];
; #pragma unroll 1
;             for (int blk = 0; blk < total; blk += 64) { const int blen = (total - blk) < 64 ? (total - blk) : 64, ng = blen / PG;
;                 const int ev = evn; const float wv = wvn;
;                 if (blk + 64 + lane < total) { evn = __builtin_nontemporal_load(FE + blk + 64 + lane); wvn = __builtin_nontemporal_load(FW + blk + 64 + lane); }
;                 const float us = USC[ev], vs = VSC[ev];
;                 float xsv = 0.f;
;                 if (ng == 16) {
;                     const bool nextfull = blk + 128 <= total;
;                     if (!pre) { PU_ROWS(A, 0); PU_ROWS(B, 1); PU_ROWS(C, 2); }
; #pragma unroll 1
;                     for (int g = 0; g < 12; g += 4) {
;                         PU_ROWS(Dq, g + 3); PU_DO(A, g); PU_ROWS(A, g + 4); PU_DO(B, g + 1); PU_ROWS(B, g + 5); PU_DO(C, g + 2); PU_ROWS(C, g + 6); PU_DO(Dq, g + 3);
;                     }
;                     PU_ROWS(Dq, 15); PU_DO(A, 12); if (nextfull) PU_ROWS_N(A, 0); PU_DO(B, 13); if (nextfull) PU_ROWS_N(B, 1); PU_DO(C, 14); if (nextfull) PU_ROWS_N(C, 2); PU_DO(Dq, 15);
.Lq_std15:
	s_waitcnt vmcnt(8)
	v_and_b32_e32 v96, 0xf0f0f0f, v48
	v_and_b32_e32 v100, 0xf0f0f0f0, v48
	v_and_b32_e32 v97, 0xf0f0f0f, v49
	v_and_b32_e32 v101, 0xf0f0f0f0, v49
	v_dot4_i32_i8 v104, v96, v64, 0
	v_dot4_i32_i8 v105, v100, v68, 0
	v_and_b32_e32 v98, 0xf0f0f0f, v50
	v_and_b32_e32 v102, 0xf0f0f0f0, v50
	v_dot4_i32_i8 v104, v97, v65, v104
	v_dot4_i32_i8 v105, v101, v69, v105
	v_and_b32_e32 v99, 0xf0f0f0f, v51
	v_and_b32_e32 v103, 0xf0f0f0f0, v51
	v_dot4_i32_i8 v104, v98, v66, v104
	v_dot4_i32_i8 v105, v102, v70, v105
	v_dot4_i32_i8 v104, v99, v67, v104
	v_dot4_i32_i8 v105, v103, v71, v105
	v_and_b32_e32 v96, 0xf0f0f0f, v52
	v_and_b32_e32 v100, 0xf0f0f0f0, v52
	v_and_b32_e32 v97, 0xf0f0f0f, v53
	v_and_b32_e32 v101, 0xf0f0f0f0, v53
	v_lshl_add_u32 v106, v104, 4, v105
	v_lshl_add_u32 v92, v106, 1, v72
	v_dot4_i32_i8 v126, v96, v64, 0
	v_dot4_i32_i8 v127, v100, v68, 0
	v_and_b32_e32 v98, 0xf0f0f0f, v54
	v_and_b32_e32 v102, 0xf0f0f0f0, v54
	v_dot4_i32_i8 v126, v97, v65, v126
	v_dot4_i32_i8 v127, v101, v69, v127
	v_and_b32_e32 v99, 0xf0f0f0f, v55
	v_and_b32_e32 v103, 0xf0f0f0f0, v55
	v_dot4_i32_i8 v126, v98, v66, v126
	v_dot4_i32_i8 v127, v102, v70, v127
	v_dot4_i32_i8 v126, v99, v67, v126
	v_dot4_i32_i8 v127, v103, v71, v127
	v_and_b32_e32 v96, 0xf0f0f0f, v56
	v_and_b32_e32 v100, 0xf0f0f0f0, v56
	v_and_b32_e32 v97, 0xf0f0f0f, v57
	v_and_b32_e32 v101, 0xf0f0f0f0, v57
	v_lshl_add_u32 v106, v126, 4, v127
	v_lshl_add_u32 v93, v106, 1, v72
	v_dot4_i32_i8 v104, v96, v64, 0
	v_dot4_i32_i8 v105, v100, v68, 0
	v_and_b32_e32 v98, 0xf0f0f0f, v58
	v_and_b32_e32 v102, 0xf0f0f0f0, v58
	v_dot4_i32_i8 v104, v97, v65, v104
	v_dot4_i32_i8 v105, v101, v69, v105
	v_and_b32_e32 v99, 0xf0f0f0f, v59
	v_and_b32_e32 v103, 0xf0f0f0f0, v59
	v_dot4_i32_i8 v104, v98, v66, v104
	v_dot4_i32_i8 v105, v102, v70, v105
	v_dot4_i32_i8 v104, v99, v67, v104
	v_dot4_i32_i8 v105, v103, v71, v105
	v_and_b32_e32 v96, 0xf0f0f0f, v60
	v_and_b32_e32 v100, 0xf0f0f0f0, v60
	v_and_b32_e32 v97, 0xf0f0f0f, v61
	v_and_b32_e32 v101, 0xf0f0f0f0, v61
	v_lshl_add_u32 v106, v104, 4, v105
	v_lshl_add_u32 v94, v106, 1, v72
	v_dot4_i32_i8 v126, v96, v64, 0
	v_dot4_i32_i8 v127, v100, v68, 0
	v_and_b32_e32 v98, 0xf0f0f0f, v62
	v_and_b32_e32 v102, 0xf0f0f0f0, v62
	v_dot4_i32_i8 v126, v97, v65, v126
	v_dot4_i32_i8 v127, v101, v69, v127
	v_and_b32_e32 v99, 0xf0f0f0f, v63
	v_and_b32_e32 v103, 0xf0f0f0f0, v63
	v_dot4_i32_i8 v126, v98, v66, v126
	v_dot4_i32_i8 v127, v102, v70, v127
	v_dot4_i32_i8 v126, v99, v67, v126
	v_dot4_i32_i8 v127, v103, v71, v127
	s_nop 0
	v_readlane_b32 s36, v76, 8
	v_readlane_b32 s5, v76, 9
	v_readlane_b32 s6, v76, 10
	v_readlane_b32 s7, v76, 11
	v_lshl_add_u32 v106, v126, 4, v127
	v_lshl_add_u32 v95, v106, 1, v72
	v_add_u32_e32 v113, s36, v206
	v_add_u32_e32 v114, s5, v206
	v_add_u32_e32 v115, s6, v206
	v_add_u32_e32 v116, s7, v206
	global_load_dwordx4 v[32:35], v113, s[52:53]
	global_load_dwordx4 v[36:39], v114, s[52:53]
	global_load_dwordx4 v[40:43], v115, s[52:53]
	global_load_dwordx4 v[44:47], v116, s[52:53]
	ds_write_b128 v107, v[92:95] offset:240
	s_lshl_b64 exec, s[22:23], 60
	v_mov_b32_e32 v87, s10
	s_mov_b64 exec, -1
	s_branch .Lq_blockend

; __device__ __forceinline__ float gelu_tanh(float x) { return pg8::gelu_tanh_f(x); }
; __device__ __forceinline__ void phase_peer_bucket(const Params& P, unsigned char* ws, int l, LAS unsigned char* lds, int bid, int G, int lane, int wave) {
;     ...
;                 int dv = 0;
;                 int dv1 = 0, dv2 = 0, dv3 = 0;
; #pragma unroll
;                 for (int r_ = 0; r_ < 64; r_ += 4) { dv += red[r_ * 68 + lane]; dv1 += red[(r_ + 1) * 68 + lane]; dv2 += red[(r_ + 2) * 68 + lane]; dv3 += red[(r_ + 3) * 68 + lane]; }
;                 dv += dv1 + dv2 + dv3;
;                 if (lane < blen) { const float hwval = wv * gelu_tanh((float)dv * us * xsv) * vs; FHW[blk + lane] = hwval; hmax = fmaxf(hmax, fabsf(hwval)); }
;             }
.Lq_blockend:
	ds_read_b32 v160, v108 offset:0
	ds_read_b32 v161, v108 offset:272
	ds_read_b32 v162, v108 offset:544
	ds_read_b32 v163, v108 offset:816
	ds_read_b32 v164, v108 offset:1088
	ds_read_b32 v165, v108 offset:1360
	ds_read_b32 v166, v108 offset:1632
	ds_read_b32 v167, v108 offset:1904
	ds_read_b32 v168, v108 offset:2176
	ds_read_b32 v169, v108 offset:2448
	ds_read_b32 v170, v108 offset:2720
	ds_read_b32 v171, v108 offset:2992
	ds_read_b32 v172, v108 offset:3264
	ds_read_b32 v173, v108 offset:3536
	ds_read_b32 v174, v108 offset:3808
	ds_read_b32 v175, v108 offset:4080
	ds_read_b32 v176, v108 offset:4352
	ds_read_b32 v177, v108 offset:4624
	ds_read_b32 v178, v108 offset:4896
	ds_read_b32 v179, v108 offset:5168
	ds_read_b32 v180, v108 offset:5440
	ds_read_b32 v181, v108 offset:5712
	ds_read_b32 v182, v108 offset:5984
	ds_read_b32 v183, v108 offset:6256
	ds_read_b32 v184, v108 offset:6528
	ds_read_b32 v185, v108 offset:6800
	ds_read_b32 v186, v108 offset:7072
	ds_read_b32 v187, v108 offset:7344
	ds_read_b32 v188, v108 offset:7616
	ds_read_b32 v189, v108 offset:7888
	ds_read_b32 v190, v108 offset:8160
	ds_read_b32 v191, v108 offset:8432
	s_waitcnt lgkmcnt(0)
	v_add3_u32 v121, v160, v161, v162
	v_add3_u32 v121, v121, v163, v164
	v_add3_u32 v121, v121, v165, v166
	v_add3_u32 v121, v121, v167, v168
	v_add3_u32 v121, v121, v169, v170
	v_add3_u32 v121, v121, v171, v172
	v_add3_u32 v121, v121, v173, v174
	v_add3_u32 v121, v121, v175, v176
	v_add3_u32 v121, v121, v177, v178
	v_add3_u32 v121, v121, v179, v180
	v_add3_u32 v121, v121, v181, v182
	v_add3_u32 v121, v121, v183, v184
	v_add3_u32 v121, v121, v185, v186
	v_add3_u32 v121, v121, v187, v188
	v_add3_u32 v121, v121, v189, v190
	v_add_u32_e32 v121, v121, v191
	ds_read_b32 v160, v108 offset:8704
	ds_read_b32 v161, v108 offset:8976
	ds_read_b32 v162, v108 offset:9248
	ds_read_b32 v163, v108 offset:9520
	ds_read_b32 v164, v108 offset:9792
	ds_read_b32 v165, v108 offset:10064
	ds_read_b32 v166, v108 offset:10336
	ds_read_b32 v167, v108 offset:10608
	ds_read_b32 v168, v108 offset:10880
	ds_read_b32 v169, v108 offset:11152
	ds_read_b32 v170, v108 offset:11424
	ds_read_b32 v171, v108 offset:11696
	ds_read_b32 v172, v108 offset:11968
	ds_read_b32 v173, v108 offset:12240
	ds_read_b32 v174, v108 offset:12512
	ds_read_b32 v175, v108 offset:12784
	ds_read_b32 v176, v108 offset:13056
	ds_read_b32 v177, v108 offset:13328
	ds_read_b32 v178, v108 offset:13600
	ds_read_b32 v179, v108 offset:13872
	ds_read_b32 v180, v108 offset:14144
	ds_read_b32 v181, v108 offset:14416
	ds_read_b32 v182, v108 offset:14688
	ds_read_b32 v183, v108 offset:14960
	ds_read_b32 v184, v108 offset:15232
	ds_read_b32 v185, v108 offset:15504
	ds_read_b32 v186, v108 offset:15776
	ds_read_b32 v187, v108 offset:16048
	ds_read_b32 v188, v108 offset:16320
	ds_read_b32 v189, v108 offset:16592
	ds_read_b32 v190, v108 offset:16864
	ds_read_b32 v191, v108 offset:17136
	s_waitcnt lgkmcnt(0)
	v_add3_u32 v121, v121, v160, v161
	v_add3_u32 v121, v121, v162, v163
	v_add3_u32 v121, v121, v164, v165
	v_add3_u32 v121, v121, v166, v167
	v_add3_u32 v121, v121, v168, v169
	v_add3_u32 v121, v121, v170, v171
	v_add3_u32 v121, v121, v172, v173
	v_add3_u32 v121, v121, v174, v175
	v_add3_u32 v121, v121, v176, v177
	v_add3_u32 v121, v121, v178, v179
	v_add3_u32 v121, v121, v180, v181
	v_add3_u32 v121, v121, v182, v183
	v_add3_u32 v121, v121, v184, v185
	v_add3_u32 v121, v121, v186, v187
	v_add3_u32 v121, v121, v188, v189
	v_add3_u32 v121, v121, v190, v191
	v_mov_b32_e32 v122, v87
	v_cvt_f32_i32_e32 v121, v121
	v_mul_f32_e32 v121, v79, v121
	v_mul_f32_e32 v121, v122, v121
	v_mul_f32_e32 v123, 0x3d372713, v121
	v_mul_f32_e32 v123, v121, v123
	v_fma_f32 v123, v121, v123, v121
	v_mul_f32_e32 v123, 0xbfcc422a, v123
	v_mul_f32_e32 v123, 0x3fb8aa3b, v123
	v_exp_f32_e32 v123, v123
	s_nop 0
	v_add_f32_e32 v123, 1.0, v123
	v_rcp_f32_e32 v123, v123
	s_nop 0
	v_mul_f32_e32 v121, v121, v123
	v_mul_f32_e32 v121, v77, v121
	v_mul_f32_e32 v123, v82, v121
	v_add_u32_e32 v124, s34, v208
	v_cmp_gt_u32_e32 vcc, s28, v124
	v_lshlrev_b32_e32 v124, 2, v124
	s_and_saveexec_b64 s[6:7], vcc
	global_store_dword v124, v123, s[16:17]
	v_max_f32_e32 v121, v233, v233
	v_max_f32_e64 v233, v121, |v123|
	s_or_b64 exec, exec, s[6:7]
	s_add_u32 s34, s34, 64
	s_cmp_lt_u32 s34, s28
	s_cbranch_scc1 .Lq_block
	s_waitcnt vmcnt(0)
	s_mov_b32 s36, 0
	s_branch .LBB0_1276
.Lq_sw0:
	s_cmp_gt_u32 s31, 31
	s_cbranch_scc1 .Lq_end
	s_mov_b32 s30, s31
	s_add_u32 s4, s30, 1
	v_readlane_b32 s35, v81, s4
	s_add_u32 s31, s30, 1

; #define PU_SX() do { int a_ = 0, b_ = 0; _Pragma("unroll") for (int q_ = 0; q_ < 4; ++q_) { a_ = __builtin_amdgcn_sdot4((int)xq[0][q_], 0x01010101, a_, false); b_ = __builtin_amdgcn_sdot4((int)xq[1][q_], 0x01010101, b_, false); } sx15 = 240 * a_ - 16 * b_; } while (0)
; __device__ __forceinline__ void phase_peer_bucket(const Params& P, unsigned char* ws, int l, LAS unsigned char* lds, int bid, int G, int lane, int wave) {
;     ...
;             int sx15; PU_SX();
.Lq_nnd15:
	v_readlane_b32 s10, v201, s30
	v_mov_b64_e32 v[64:65], v[128:129]
	v_mov_b64_e32 v[68:69], v[132:133]
	v_mov_b64_e32 v[66:67], v[130:131]
	v_mov_b64_e32 v[70:71], v[134:135]
	v_dot4_i32_i8 v118, v128, s65, 0
	v_dot4_i32_i8 v119, v132, s65, 0
	v_dot4_i32_i8 v118, v129, s65, v118
	v_dot4_i32_i8 v119, v133, s65, v119
	v_dot4_i32_i8 v118, v130, s65, v118
	v_dot4_i32_i8 v119, v134, s65, v119
	v_dot4_i32_i8 v118, v131, s65, v118
	v_dot4_i32_i8 v119, v135, s65, v119
	s_nop 2
	v_mul_i32_i24_e32 v118, 0xf0, v118
	v_lshlrev_b32_e32 v119, 4, v119
	v_sub_u32_e32 v72, v119, v118
	s_branch .Lq_swret0

; #define PU_SX() do { int a_ = 0, b_ = 0; _Pragma("unroll") for (int q_ = 0; q_ < 4; ++q_) { a_ = __builtin_amdgcn_sdot4((int)xq[0][q_], 0x01010101, a_, false); b_ = __builtin_amdgcn_sdot4((int)xq[1][q_], 0x01010101, b_, false); } sx15 = 240 * a_ - 16 * b_; } while (0)
; __device__ __forceinline__ void phase_peer_bucket(const Params& P, unsigned char* ws, int l, LAS unsigned char* lds, int bid, int G, int lane, int wave) {
;     ...
;             int sx15; PU_SX();
.Lq_nnd16:
	v_readlane_b32 s10, v201, s30
	v_mov_b64_e32 v[64:65], v[136:137]
	v_mov_b64_e32 v[68:69], v[140:141]
	v_mov_b64_e32 v[66:67], v[138:139]
	v_mov_b64_e32 v[70:71], v[142:143]
	v_dot4_i32_i8 v118, v136, s65, 0
	v_dot4_i32_i8 v119, v140, s65, 0
	v_dot4_i32_i8 v118, v137, s65, v118
	v_dot4_i32_i8 v119, v141, s65, v119
	v_dot4_i32_i8 v118, v138, s65, v118
	v_dot4_i32_i8 v119, v142, s65, v119
	v_dot4_i32_i8 v118, v139, s65, v118
	v_dot4_i32_i8 v119, v143, s65, v119
	s_nop 2
	v_mul_i32_i24_e32 v118, 0xf0, v118
	v_lshlrev_b32_e32 v119, 4, v119
	v_sub_u32_e32 v72, v119, v118
	s_branch .Lq_swret1

; #define PU_SX() do { int a_ = 0, b_ = 0; _Pragma("unroll") for (int q_ = 0; q_ < 4; ++q_) { a_ = __builtin_amdgcn_sdot4((int)xq[0][q_], 0x01010101, a_, false); b_ = __builtin_amdgcn_sdot4((int)xq[1][q_], 0x01010101, b_, false); } sx15 = 240 * a_ - 16 * b_; } while (0)
; __device__ __forceinline__ void phase_peer_bucket(const Params& P, unsigned char* ws, int l, LAS unsigned char* lds, int bid, int G, int lane, int wave) {
;     ...
;             int sx15; PU_SX();
.Lq_nnd17:
	v_readlane_b32 s10, v201, s30
	v_mov_b64_e32 v[64:65], v[144:145]
	v_mov_b64_e32 v[68:69], v[148:149]
	v_mov_b64_e32 v[66:67], v[146:147]
	v_mov_b64_e32 v[70:71], v[150:151]
	v_dot4_i32_i8 v118, v144, s65, 0
	v_dot4_i32_i8 v119, v148, s65, 0
	v_dot4_i32_i8 v118, v145, s65, v118
	v_dot4_i32_i8 v119, v149, s65, v119
	v_dot4_i32_i8 v118, v146, s65, v118
	v_dot4_i32_i8 v119, v150, s65, v119
	v_dot4_i32_i8 v118, v147, s65, v118
	v_dot4_i32_i8 v119, v151, s65, v119
	s_nop 2
	v_mul_i32_i24_e32 v118, 0xf0, v118
	v_lshlrev_b32_e32 v119, 4, v119
	v_sub_u32_e32 v72, v119, v118
	s_branch .Lq_swret2

; #define PU_SX() do { int a_ = 0, b_ = 0; _Pragma("unroll") for (int q_ = 0; q_ < 4; ++q_) { a_ = __builtin_amdgcn_sdot4((int)xq[0][q_], 0x01010101, a_, false); b_ = __builtin_amdgcn_sdot4((int)xq[1][q_], 0x01010101, b_, false); } sx15 = 240 * a_ - 16 * b_; } while (0)
; __device__ __forceinline__ void phase_peer_bucket(const Params& P, unsigned char* ws, int l, LAS unsigned char* lds, int bid, int G, int lane, int wave) {
;     ...
;             int sx15; PU_SX();
.Lq_nnd18:
	v_readlane_b32 s10, v201, s30
	v_mov_b64_e32 v[64:65], v[152:153]
	v_mov_b64_e32 v[68:69], v[156:157]
	v_mov_b64_e32 v[66:67], v[154:155]
	v_mov_b64_e32 v[70:71], v[158:159]
	v_dot4_i32_i8 v118, v152, s65, 0
	v_dot4_i32_i8 v119, v156, s65, 0
	v_dot4_i32_i8 v118, v153, s65, v118
	v_dot4_i32_i8 v119, v157, s65, v119
	v_dot4_i32_i8 v118, v154, s65, v118
	v_dot4_i32_i8 v119, v158, s65, v119
	v_dot4_i32_i8 v118, v155, s65, v118
	v_dot4_i32_i8 v119, v159, s65, v119
	s_nop 2
	v_mul_i32_i24_e32 v118, 0xf0, v118
	v_lshlrev_b32_e32 v119, 4, v119
	v_sub_u32_e32 v72, v119, v118
	s_branch .Lq_swret3

.Lq_stx0:
	s_lshl_b32 s5, s50, 11
	s_add_u32 s6, s26, s5
	s_addc_u32 s7, s27, 0
	global_load_dwordx4 v[128:131], v206, s[6:7] nt
	global_load_dwordx4 v[132:135], v206, s[6:7] offset:1024 nt
	s_add_u32 s50, s50, 1

.Lq_stx1:
	s_lshl_b32 s5, s50, 11
	s_add_u32 s6, s26, s5
	s_addc_u32 s7, s27, 0
	global_load_dwordx4 v[136:139], v206, s[6:7] nt
	global_load_dwordx4 v[140:143], v206, s[6:7] offset:1024 nt
	s_add_u32 s50, s50, 1

.Lq_stx2:
	s_lshl_b32 s5, s50, 11
	s_add_u32 s6, s26, s5
	s_addc_u32 s7, s27, 0
	global_load_dwordx4 v[144:147], v206, s[6:7] nt
	global_load_dwordx4 v[148:151], v206, s[6:7] offset:1024 nt
	s_add_u32 s50, s50, 1

.Lq_stx3:
	s_lshl_b32 s5, s50, 11
	s_add_u32 s6, s26, s5
	s_addc_u32 s7, s27, 0
	global_load_dwordx4 v[152:155], v206, s[6:7] nt
	global_load_dwordx4 v[156:159], v206, s[6:7] offset:1024 nt
	s_add_u32 s50, s50, 1

; #define VM_WAIT() asm volatile("s_waitcnt vmcnt(0)" ::: "memory")
; __device__ __forceinline__ void phase_peer_bucket(const Params& P, unsigned char* ws, int l, LAS unsigned char* lds, int bid, int G, int lane, int wave) {
;     ...
;         VM_WAIT();
;         hmax = wave_max_dpp(hmax);
;         const int hex_ = (__float_as_int(hmax) >> 23) & 0xff;
;         const float hs = (hmax > 0.f) ? __int_as_float((251 - hex_) << 23) : 1.f, hinv = (hmax > 0.f) ? __int_as_float((hex_ + 3) << 23) : 1.f;
.Lq_tr62:
	s_branch .Lq_std15
.LBB0_1276:
	v_mov_b32_dpp v0, v233 quad_perm:[1,0,3,2] row_mask:0xf bank_mask:0xf bound_ctrl:1
	v_max_f32_e32 v0, v0, v0
	v_max_f32_e32 v1, v233, v233
	v_max_f32_e32 v0, v1, v0
	v_readlane_b32 s4, v253, 24
	s_add_u32 s4, s12, s4
	v_mov_b32_dpp v1, v0 quad_perm:[2,3,0,1] row_mask:0xf bank_mask:0xf bound_ctrl:1
	v_max_f32_e32 v1, v1, v1
	v_max_f32_e32 v0, v0, v1
	s_addc_u32 s5, s13, 0
	s_add_u32 s10, s4, 0x5b000000
	v_mov_b32_dpp v1, v0 row_half_mirror row_mask:0xf bank_mask:0xf bound_ctrl:1
	v_max_f32_e32 v1, v1, v1
	v_max_f32_e32 v0, v0, v1
	s_addc_u32 s11, s5, 0
	s_mov_b32 s9, s37
	v_mov_b32_dpp v1, v0 row_mirror row_mask:0xf bank_mask:0xf bound_ctrl:1
	v_max_f32_e32 v1, v1, v1
	v_max_f32_e32 v0, v0, v1
	s_waitcnt vmcnt(0)
	s_mov_b32 s26, 0
	v_readlane_b32 s6, v0, 32
	v_readlane_b32 s7, v0, 48
	v_readlane_b32 s4, v0, 0
	v_max_f32_e64 v1, s6, s6
	v_readlane_b32 s6, v253, 31
	v_readlane_b32 s5, v0, 16
	v_max_f32_e64 v0, s7, s7
	s_add_u32 s18, s12, s6
	v_max_f32_e32 v0, v1, v0
	v_mov_b32_e32 v1, s5
	s_addc_u32 s19, s13, 0
	s_lshl_b64 s[6:7], s[8:9], 2
	v_max3_f32 v1, s4, v1, v0
	s_add_u32 s18, s18, s6
	v_and_b32_e32 v0, 0x7f800000, v1
	s_addc_u32 s19, s19, s7
	s_lshl_b32 s6, s29, 5
	v_readlane_b32 s7, v253, 34
	v_add_u32_e32 v2, 0x1800000, v0
	v_cmp_lt_f32_e64 s[4:5], 0, v1
	s_add_i32 s6, s7, s6
	v_cmp_eq_u32_e64 s[38:39], 0, v208
	v_cndmask_b32_e64 v134, 1.0, v2, s[4:5]
	s_lshl_b32 s9, s6, 10
	s_branch .LBB0_1279
